# plus removal of the redundant mid-segment s_setprio 0/1 pairs in GEMM MFMA segments
# speedup vs baseline: 1.0106x; 1.0006x over previous
.LBB0_243:
	ds_read_b128 v[74:77], v201
	ds_read_b128 v[78:81], v201 offset:1024
	ds_read_b128 v[82:85], v201 offset:2048
	ds_read_b128 v[86:89], v201 offset:3072
	ds_read_b128 v[164:167], v202
	ds_read_b128 v[168:171], v202 offset:1024
	ds_read_b128 v[172:175], v202 offset:2048
	ds_read_b128 v[176:179], v202 offset:3072
	s_add_u32 s26, s24, 0xfff80080
	s_addc_u32 s27, s25, -1
	s_cmp_eq_u32 s19, 28
	s_cselect_b32 s29, s21, s27
	s_cselect_b32 s28, s20, s26
	s_cselect_b32 s27, s23, s17
	s_cselect_b32 s26, s22, s7
	v_lshl_add_u64 v[228:229], s[24:25], 0, v[156:157]
	s_add_i32 m0, s41, 0xc000
	ds_read_b128 v[180:183], v203
	ds_read_b128 v[184:187], v203 offset:1024
	ds_read_b128 v[204:207], v203 offset:2048
	ds_read_b128 v[208:211], v203 offset:3072
	ds_read_b128 v[212:215], v203 offset:4096
	ds_read_b128 v[216:219], v203 offset:5120
	ds_read_b128 v[220:223], v203 offset:6144
	ds_read_b128 v[224:227], v203 offset:7168
	global_load_lds_dwordx4 v[228:229], off
	v_lshl_add_u64 v[228:229], s[24:25], 0, v[158:159]
	s_add_i32 m0, s41, 0xe000
	s_nop 0
	global_load_lds_dwordx4 v[228:229], off
	s_waitcnt vmcnt(8)
	s_waitcnt lgkmcnt(0)
	s_barrier
	s_setprio 1
	s_waitcnt lgkmcnt(0)
	v_mfma_f32_16x16x32_bf16 v[142:145], v[74:77], v[180:183], v[142:145]
	v_mfma_f32_16x16x32_bf16 v[138:141], v[82:85], v[180:183], v[138:141]
	v_mfma_f32_16x16x32_bf16 v[126:129], v[74:77], v[204:207], v[126:129]
	v_mfma_f32_16x16x32_bf16 v[122:125], v[82:85], v[204:207], v[122:125]
	v_mfma_f32_16x16x32_bf16 v[110:113], v[74:77], v[212:215], v[110:113]
	v_mfma_f32_16x16x32_bf16 v[106:109], v[82:85], v[212:215], v[106:109]
	v_mfma_f32_16x16x32_bf16 v[94:97], v[74:77], v[220:223], v[94:97]
	v_mfma_f32_16x16x32_bf16 v[90:93], v[82:85], v[220:223], v[90:93]
	v_mfma_f32_16x16x32_bf16 v[142:145], v[78:81], v[184:187], v[142:145]
	v_mfma_f32_16x16x32_bf16 v[138:141], v[86:89], v[184:187], v[138:141]
	v_mfma_f32_16x16x32_bf16 v[126:129], v[78:81], v[208:211], v[126:129]
	v_mfma_f32_16x16x32_bf16 v[122:125], v[86:89], v[208:211], v[122:125]
	v_mfma_f32_16x16x32_bf16 v[110:113], v[78:81], v[216:219], v[110:113]
	v_mfma_f32_16x16x32_bf16 v[106:109], v[86:89], v[216:219], v[106:109]
	v_mfma_f32_16x16x32_bf16 v[94:97], v[78:81], v[224:227], v[94:97]
	v_mfma_f32_16x16x32_bf16 v[90:93], v[86:89], v[224:227], v[90:93]
	v_mfma_f32_16x16x32_bf16 v[134:137], v[164:167], v[180:183], v[134:137]
	v_mfma_f32_16x16x32_bf16 v[130:133], v[172:175], v[180:183], v[130:133]
	v_mfma_f32_16x16x32_bf16 v[118:121], v[164:167], v[204:207], v[118:121]
	v_mfma_f32_16x16x32_bf16 v[114:117], v[172:175], v[204:207], v[114:117]
	v_mfma_f32_16x16x32_bf16 v[102:105], v[164:167], v[212:215], v[102:105]
	v_mfma_f32_16x16x32_bf16 v[98:101], v[172:175], v[212:215], v[98:101]
	v_mfma_f32_16x16x32_bf16 v[70:73], v[164:167], v[220:223], v[70:73]
	v_mfma_f32_16x16x32_bf16 v[66:69], v[172:175], v[220:223], v[66:69]
	v_mfma_f32_16x16x32_bf16 v[134:137], v[168:171], v[184:187], v[134:137]
	v_mfma_f32_16x16x32_bf16 v[130:133], v[176:179], v[184:187], v[130:133]
	v_mfma_f32_16x16x32_bf16 v[118:121], v[168:171], v[208:211], v[118:121]
	v_mfma_f32_16x16x32_bf16 v[114:117], v[176:179], v[208:211], v[114:117]
	v_mfma_f32_16x16x32_bf16 v[102:105], v[168:171], v[216:219], v[102:105]
	v_mfma_f32_16x16x32_bf16 v[98:101], v[176:179], v[216:219], v[98:101]
	v_mfma_f32_16x16x32_bf16 v[70:73], v[168:171], v[224:227], v[70:73]
	v_mfma_f32_16x16x32_bf16 v[66:69], v[176:179], v[224:227], v[66:69]
	s_setprio 0
	s_barrier
	s_add_i32 s30, s53, s40
	v_lshl_add_u64 v[228:229], s[26:27], 0, v[148:149]
	s_mov_b32 m0, s30
	ds_read_b128 v[180:183], v203 offset:16384
	ds_read_b128 v[184:187], v203 offset:17408
	ds_read_b128 v[204:207], v203 offset:18432
	ds_read_b128 v[208:211], v203 offset:19456
	ds_read_b128 v[212:215], v203 offset:20480
	ds_read_b128 v[216:219], v203 offset:21504
	ds_read_b128 v[220:223], v203 offset:22528
	ds_read_b128 v[224:227], v203 offset:23552
	global_load_lds_dwordx4 v[228:229], off
	s_add_i32 m0, s30, 0x2000
	s_add_u32 s30, s26, 0x80000
	v_lshl_add_u64 v[230:231], s[26:27], 0, v[152:153]
	s_addc_u32 s31, s27, 0
	s_add_i32 s34, s54, s40
	global_load_lds_dwordx4 v[230:231], off
	v_lshl_add_u64 v[232:233], s[30:31], 0, v[148:149]
	s_mov_b32 m0, s34
	v_lshl_add_u64 v[234:235], s[28:29], 0, v[150:151]
	global_load_lds_dwordx4 v[232:233], off
	v_lshl_add_u64 v[232:233], s[30:31], 0, v[152:153]
	s_add_i32 m0, s34, 0x2000
	s_nop 0
	global_load_lds_dwordx4 v[232:233], off
	s_waitcnt vmcnt(6)
	s_waitcnt lgkmcnt(0)
	s_barrier
	s_setprio 1
	s_waitcnt lgkmcnt(0)
	v_mfma_f32_16x16x32_bf16 v[62:65], v[74:77], v[180:183], v[62:65]
	v_mfma_f32_16x16x32_bf16 v[58:61], v[82:85], v[180:183], v[58:61]
	v_mfma_f32_16x16x32_bf16 v[46:49], v[74:77], v[204:207], v[46:49]
	v_mfma_f32_16x16x32_bf16 v[42:45], v[82:85], v[204:207], v[42:45]
	v_mfma_f32_16x16x32_bf16 v[30:33], v[74:77], v[212:215], v[30:33]
	v_mfma_f32_16x16x32_bf16 v[26:29], v[82:85], v[212:215], v[26:29]
	v_mfma_f32_16x16x32_bf16 v[14:17], v[74:77], v[220:223], v[14:17]
	v_mfma_f32_16x16x32_bf16 v[10:13], v[82:85], v[220:223], v[10:13]
	v_mfma_f32_16x16x32_bf16 v[62:65], v[78:81], v[184:187], v[62:65]
	v_lshl_add_u64 v[232:233], s[28:29], 0, v[146:147]
	s_mov_b32 m0, s41
	s_nop 0
	global_load_lds_dwordx4 v[232:233], off
	v_mfma_f32_16x16x32_bf16 v[58:61], v[86:89], v[184:187], v[58:61]
	v_mfma_f32_16x16x32_bf16 v[46:49], v[78:81], v[208:211], v[46:49]
	v_mfma_f32_16x16x32_bf16 v[42:45], v[86:89], v[208:211], v[42:45]
	v_mfma_f32_16x16x32_bf16 v[30:33], v[78:81], v[216:219], v[30:33]
	v_mfma_f32_16x16x32_bf16 v[26:29], v[86:89], v[216:219], v[26:29]
	v_mfma_f32_16x16x32_bf16 v[14:17], v[78:81], v[224:227], v[14:17]
	v_mfma_f32_16x16x32_bf16 v[10:13], v[86:89], v[224:227], v[10:13]
	v_mfma_f32_16x16x32_bf16 v[54:57], v[164:167], v[180:183], v[54:57]
	v_mfma_f32_16x16x32_bf16 v[50:53], v[172:175], v[180:183], v[50:53]
	v_mfma_f32_16x16x32_bf16 v[38:41], v[164:167], v[204:207], v[38:41]
	v_mfma_f32_16x16x32_bf16 v[34:37], v[172:175], v[204:207], v[34:37]
	v_mfma_f32_16x16x32_bf16 v[22:25], v[164:167], v[212:215], v[22:25]
	s_mov_b32 m0, s42
	s_nop 0
	global_load_lds_dwordx4 v[234:235], off
	v_mfma_f32_16x16x32_bf16 v[18:21], v[172:175], v[212:215], v[18:21]
	v_mfma_f32_16x16x32_bf16 v[6:9], v[164:167], v[220:223], v[6:9]
	v_mfma_f32_16x16x32_bf16 v[2:5], v[172:175], v[220:223], v[2:5]
	v_mfma_f32_16x16x32_bf16 v[54:57], v[168:171], v[184:187], v[54:57]
	v_mfma_f32_16x16x32_bf16 v[50:53], v[176:179], v[184:187], v[50:53]
	v_mfma_f32_16x16x32_bf16 v[38:41], v[168:171], v[208:211], v[38:41]
	v_mfma_f32_16x16x32_bf16 v[34:37], v[176:179], v[208:211], v[34:37]
	v_mfma_f32_16x16x32_bf16 v[22:25], v[168:171], v[216:219], v[22:25]
	v_mfma_f32_16x16x32_bf16 v[18:21], v[176:179], v[216:219], v[18:21]
	v_mfma_f32_16x16x32_bf16 v[6:9], v[168:171], v[224:227], v[6:9]
	v_mfma_f32_16x16x32_bf16 v[2:5], v[176:179], v[224:227], v[2:5]
	s_setprio 0
	s_barrier
	s_add_i32 s30, 0, 0x18000
	s_add_i32 s31, 0, 0x1c000
	v_add_u32_e32 v86, s30, v200
	v_add_u32_e32 v154, s31, v200
	ds_read_b128 v[74:77], v86
	ds_read_b128 v[78:81], v86 offset:1024
	ds_read_b128 v[82:85], v86 offset:2048
	ds_read_b128 v[86:89], v86 offset:3072
	ds_read_b128 v[164:167], v154
	ds_read_b128 v[168:171], v154 offset:1024
	ds_read_b128 v[172:175], v154 offset:2048
	ds_read_b128 v[176:179], v154 offset:3072
	s_add_u32 s28, s28, 0x80000
	s_addc_u32 s29, s29, 0
	s_mov_b32 m0, s43
	v_lshl_add_u64 v[236:237], s[28:29], 0, v[146:147]
	ds_read_b128 v[180:183], v203 offset:32768
	ds_read_b128 v[184:187], v203 offset:33792
	ds_read_b128 v[204:207], v203 offset:34816
	ds_read_b128 v[208:211], v203 offset:35840
	ds_read_b128 v[212:215], v203 offset:36864
	ds_read_b128 v[216:219], v203 offset:37888
	ds_read_b128 v[220:223], v203 offset:38912
	ds_read_b128 v[224:227], v203 offset:39936
	global_load_lds_dwordx4 v[236:237], off
	v_lshl_add_u64 v[236:237], s[28:29], 0, v[150:151]
	s_mov_b32 m0, s44
	s_nop 0
	global_load_lds_dwordx4 v[236:237], off
	s_waitcnt vmcnt(8)
	s_waitcnt lgkmcnt(0)
	s_barrier
	s_setprio 1
	s_waitcnt lgkmcnt(0)
	v_mfma_f32_16x16x32_bf16 v[142:145], v[74:77], v[180:183], v[142:145]
	v_mfma_f32_16x16x32_bf16 v[138:141], v[82:85], v[180:183], v[138:141]
	v_mfma_f32_16x16x32_bf16 v[126:129], v[74:77], v[204:207], v[126:129]
	v_mfma_f32_16x16x32_bf16 v[122:125], v[82:85], v[204:207], v[122:125]
	v_mfma_f32_16x16x32_bf16 v[110:113], v[74:77], v[212:215], v[110:113]
	v_mfma_f32_16x16x32_bf16 v[106:109], v[82:85], v[212:215], v[106:109]
	v_mfma_f32_16x16x32_bf16 v[94:97], v[74:77], v[220:223], v[94:97]
	v_mfma_f32_16x16x32_bf16 v[90:93], v[82:85], v[220:223], v[90:93]
	v_mfma_f32_16x16x32_bf16 v[142:145], v[78:81], v[184:187], v[142:145]
	v_mfma_f32_16x16x32_bf16 v[138:141], v[86:89], v[184:187], v[138:141]
	v_mfma_f32_16x16x32_bf16 v[126:129], v[78:81], v[208:211], v[126:129]
	v_mfma_f32_16x16x32_bf16 v[122:125], v[86:89], v[208:211], v[122:125]
	v_mfma_f32_16x16x32_bf16 v[110:113], v[78:81], v[216:219], v[110:113]
	v_mfma_f32_16x16x32_bf16 v[106:109], v[86:89], v[216:219], v[106:109]
	v_mfma_f32_16x16x32_bf16 v[94:97], v[78:81], v[224:227], v[94:97]
	v_mfma_f32_16x16x32_bf16 v[90:93], v[86:89], v[224:227], v[90:93]
	v_mfma_f32_16x16x32_bf16 v[134:137], v[164:167], v[180:183], v[134:137]
	v_mfma_f32_16x16x32_bf16 v[130:133], v[172:175], v[180:183], v[130:133]
	v_mfma_f32_16x16x32_bf16 v[118:121], v[164:167], v[204:207], v[118:121]
	v_mfma_f32_16x16x32_bf16 v[114:117], v[172:175], v[204:207], v[114:117]
	v_mfma_f32_16x16x32_bf16 v[102:105], v[164:167], v[212:215], v[102:105]
	v_mfma_f32_16x16x32_bf16 v[98:101], v[172:175], v[212:215], v[98:101]
	v_mfma_f32_16x16x32_bf16 v[70:73], v[164:167], v[220:223], v[70:73]
	v_mfma_f32_16x16x32_bf16 v[66:69], v[172:175], v[220:223], v[66:69]
	v_mfma_f32_16x16x32_bf16 v[134:137], v[168:171], v[184:187], v[134:137]
	v_mfma_f32_16x16x32_bf16 v[130:133], v[176:179], v[184:187], v[130:133]
	v_mfma_f32_16x16x32_bf16 v[118:121], v[168:171], v[208:211], v[118:121]
	v_mfma_f32_16x16x32_bf16 v[114:117], v[176:179], v[208:211], v[114:117]
	v_mfma_f32_16x16x32_bf16 v[102:105], v[168:171], v[216:219], v[102:105]
	v_mfma_f32_16x16x32_bf16 v[98:101], v[176:179], v[216:219], v[98:101]
	v_mfma_f32_16x16x32_bf16 v[70:73], v[168:171], v[224:227], v[70:73]
	v_mfma_f32_16x16x32_bf16 v[66:69], v[176:179], v[224:227], v[66:69]
	s_setprio 0
	s_barrier
	s_add_i32 s28, s30, s40
	v_lshl_add_u64 v[228:229], v[228:229], 0, s[12:13]
	s_mov_b32 m0, s28
	ds_read_b128 v[180:183], v203 offset:49152
	ds_read_b128 v[184:187], v203 offset:50176
	ds_read_b128 v[204:207], v203 offset:51200
	ds_read_b128 v[208:211], v203 offset:52224
	ds_read_b128 v[212:215], v203 offset:53248
	ds_read_b128 v[216:219], v203 offset:54272
	ds_read_b128 v[220:223], v203 offset:55296
	ds_read_b128 v[224:227], v203 offset:56320
	global_load_lds_dwordx4 v[228:229], off
	s_add_i32 m0, s28, 0x2000
	s_add_u32 s26, s26, 0x80080
	v_lshl_add_u64 v[228:229], v[230:231], 0, s[12:13]
	s_addc_u32 s27, s27, 0
	s_add_i32 s28, s31, s40
	global_load_lds_dwordx4 v[228:229], off
	v_lshl_add_u64 v[228:229], s[26:27], 0, v[148:149]
	s_mov_b32 m0, s28
	s_nop 0
	global_load_lds_dwordx4 v[228:229], off
	v_lshl_add_u64 v[228:229], s[26:27], 0, v[152:153]
	s_add_i32 m0, s28, 0x2000
	s_nop 0
	global_load_lds_dwordx4 v[228:229], off
	s_waitcnt vmcnt(6)
	s_waitcnt lgkmcnt(0)
	s_barrier
	s_setprio 1
	s_waitcnt lgkmcnt(0)
	v_mfma_f32_16x16x32_bf16 v[62:65], v[74:77], v[180:183], v[62:65]
	v_mfma_f32_16x16x32_bf16 v[58:61], v[82:85], v[180:183], v[58:61]
	v_mfma_f32_16x16x32_bf16 v[46:49], v[74:77], v[204:207], v[46:49]
	v_mfma_f32_16x16x32_bf16 v[42:45], v[82:85], v[204:207], v[42:45]
	v_mfma_f32_16x16x32_bf16 v[30:33], v[74:77], v[212:215], v[30:33]
	v_mfma_f32_16x16x32_bf16 v[26:29], v[82:85], v[212:215], v[26:29]
	v_mfma_f32_16x16x32_bf16 v[14:17], v[74:77], v[220:223], v[14:17]
	v_mfma_f32_16x16x32_bf16 v[10:13], v[82:85], v[220:223], v[10:13]
	v_mfma_f32_16x16x32_bf16 v[62:65], v[78:81], v[184:187], v[62:65]
	v_lshl_add_u64 v[228:229], v[232:233], 0, s[12:13]
	s_mov_b32 m0, s46
	s_nop 0
	global_load_lds_dwordx4 v[228:229], off
	v_mfma_f32_16x16x32_bf16 v[58:61], v[86:89], v[184:187], v[58:61]
	v_mfma_f32_16x16x32_bf16 v[46:49], v[78:81], v[208:211], v[46:49]
	v_mfma_f32_16x16x32_bf16 v[42:45], v[86:89], v[208:211], v[42:45]
	v_mfma_f32_16x16x32_bf16 v[30:33], v[78:81], v[216:219], v[30:33]
	v_mfma_f32_16x16x32_bf16 v[26:29], v[86:89], v[216:219], v[26:29]
	v_mfma_f32_16x16x32_bf16 v[14:17], v[78:81], v[224:227], v[14:17]
	v_mfma_f32_16x16x32_bf16 v[10:13], v[86:89], v[224:227], v[10:13]
	v_mfma_f32_16x16x32_bf16 v[54:57], v[164:167], v[180:183], v[54:57]
	v_mfma_f32_16x16x32_bf16 v[50:53], v[172:175], v[180:183], v[50:53]
	v_mfma_f32_16x16x32_bf16 v[38:41], v[164:167], v[204:207], v[38:41]
	v_mfma_f32_16x16x32_bf16 v[34:37], v[172:175], v[204:207], v[34:37]
	v_mfma_f32_16x16x32_bf16 v[22:25], v[164:167], v[212:215], v[22:25]
	v_lshl_add_u64 v[228:229], v[234:235], 0, s[12:13]
	s_mov_b32 m0, s47
	s_nop 0
	global_load_lds_dwordx4 v[228:229], off
	v_mfma_f32_16x16x32_bf16 v[18:21], v[172:175], v[212:215], v[18:21]
	v_mfma_f32_16x16x32_bf16 v[6:9], v[164:167], v[220:223], v[6:9]
	v_mfma_f32_16x16x32_bf16 v[2:5], v[172:175], v[220:223], v[2:5]
	v_mfma_f32_16x16x32_bf16 v[54:57], v[168:171], v[184:187], v[54:57]
	v_mfma_f32_16x16x32_bf16 v[50:53], v[176:179], v[184:187], v[50:53]
	v_mfma_f32_16x16x32_bf16 v[38:41], v[168:171], v[208:211], v[38:41]
	v_mfma_f32_16x16x32_bf16 v[34:37], v[176:179], v[208:211], v[34:37]
	v_mfma_f32_16x16x32_bf16 v[22:25], v[168:171], v[216:219], v[22:25]
	v_mfma_f32_16x16x32_bf16 v[18:21], v[176:179], v[216:219], v[18:21]
	v_mfma_f32_16x16x32_bf16 v[6:9], v[168:171], v[224:227], v[6:9]
	v_mfma_f32_16x16x32_bf16 v[2:5], v[176:179], v[224:227], v[2:5]
	s_setprio 0
	s_barrier
	s_add_i32 s19, s19, 2
	s_add_u32 s24, s24, 0x100
	s_addc_u32 s25, s25, 0
	s_add_u32 s7, s7, 0x100
	s_addc_u32 s17, s17, 0
	s_cmp_gt_u32 s19, 29
	s_cbranch_scc0 .LBB0_243
	s_and_b64 vcc, exec, s[14:15]
	s_cbranch_vccz .LBB0_246
	s_barrier

.LBB0_373:
	ds_read_b128 v[170:173], v1
	ds_read_b128 v[174:177], v156
	ds_read_b128 v[178:181], v157
	ds_read_b128 v[182:185], v158
	ds_read_b128 v[186:189], v159
	ds_read_b128 v[190:193], v160
	ds_read_b128 v[194:197], v161
	ds_read_b128 v[198:201], v162
	s_add_u32 s36, s6, 0xfffc0080
	s_addc_u32 s37, s7, -1
	s_cmp_eq_u32 s29, 12
	s_cselect_b32 s39, s31, s37
	s_cselect_b32 s38, s30, s36
	s_cselect_b32 s37, s35, s27
	s_cselect_b32 s36, s34, s9
	v_lshl_add_u64 v[148:149], s[6:7], 0, v[140:141]
	s_add_i32 m0, s43, 0xc000
	ds_read_b128 v[202:205], v163
	ds_read_b128 v[210:213], v163 offset:1024
	ds_read_b128 v[206:209], v164
	ds_read_b128 v[214:217], v164 offset:1024
	ds_read_b128 v[218:221], v163 offset:4096
	ds_read_b128 v[226:229], v163 offset:5120
	ds_read_b128 v[222:225], v164 offset:4096
	ds_read_b128 v[230:233], v164 offset:5120
	global_load_lds_dwordx4 v[148:149], off
	v_lshl_add_u64 v[148:149], s[6:7], 0, v[142:143]
	s_add_i32 m0, s43, 0xe000
	s_nop 0
	global_load_lds_dwordx4 v[148:149], off
	s_waitcnt vmcnt(8)
	s_waitcnt lgkmcnt(0)
	s_barrier
	s_setprio 1
	s_waitcnt lgkmcnt(0)
	v_mfma_scale_f32_32x32x64_f8f6f4 v[114:129], v[170:177], v[202:209], v[114:129], v165, v165 op_sel_hi:[0,0,0]
	v_mfma_scale_f32_32x32x64_f8f6f4 v[82:97], v[170:177], v[218:225], v[82:97], v165, v165 op_sel_hi:[0,0,0]
	v_mfma_scale_f32_32x32x64_f8f6f4 v[114:129], v[178:185], v[210:217], v[114:129], v165, v165 op_sel_hi:[0,0,0]
	v_mfma_scale_f32_32x32x64_f8f6f4 v[82:97], v[178:185], v[226:233], v[82:97], v165, v165 op_sel_hi:[0,0,0]
	v_mfma_scale_f32_32x32x64_f8f6f4 v[98:113], v[186:193], v[202:209], v[98:113], v165, v165 op_sel_hi:[0,0,0]
	v_mfma_scale_f32_32x32x64_f8f6f4 v[66:81], v[186:193], v[218:225], v[66:81], v165, v165 op_sel_hi:[0,0,0]
	v_mfma_scale_f32_32x32x64_f8f6f4 v[98:113], v[194:201], v[210:217], v[98:113], v165, v165 op_sel_hi:[0,0,0]
	v_mfma_scale_f32_32x32x64_f8f6f4 v[66:81], v[194:201], v[226:233], v[66:81], v165, v165 op_sel_hi:[0,0,0]
	s_setprio 0
	s_barrier
	s_add_i32 s55, s51, s42
	v_lshl_add_u64 v[148:149], s[36:37], 0, v[132:133]
	s_mov_b32 m0, s55
	ds_read_b128 v[202:205], v163 offset:16384
	ds_read_b128 v[210:213], v163 offset:17408
	ds_read_b128 v[206:209], v164 offset:16384
	ds_read_b128 v[214:217], v164 offset:17408
	ds_read_b128 v[218:221], v163 offset:20480
	ds_read_b128 v[226:229], v163 offset:21504
	ds_read_b128 v[222:225], v164 offset:20480
	ds_read_b128 v[230:233], v164 offset:21504
	global_load_lds_dwordx4 v[148:149], off
	s_add_i32 m0, s55, 0x2000
	s_add_u32 s56, s36, 0x40000
	v_lshl_add_u64 v[150:151], s[36:37], 0, v[136:137]
	s_addc_u32 s57, s37, 0
	s_add_i32 s55, s52, s42
	global_load_lds_dwordx4 v[150:151], off
	v_lshl_add_u64 v[152:153], s[56:57], 0, v[132:133]
	s_mov_b32 m0, s55
	v_lshl_add_u64 v[234:235], s[38:39], 0, v[134:135]
	global_load_lds_dwordx4 v[152:153], off
	v_lshl_add_u64 v[152:153], s[56:57], 0, v[136:137]
	s_add_i32 m0, s55, 0x2000
	s_nop 0
	global_load_lds_dwordx4 v[152:153], off
	s_waitcnt vmcnt(6)
	s_waitcnt lgkmcnt(0)
	s_barrier
	s_setprio 1
	s_waitcnt lgkmcnt(0)
	v_mfma_scale_f32_32x32x64_f8f6f4 v[50:65], v[170:177], v[202:209], v[50:65], v165, v165 op_sel_hi:[0,0,0]
	v_mfma_scale_f32_32x32x64_f8f6f4 v[18:33], v[170:177], v[218:225], v[18:33], v165, v165 op_sel_hi:[0,0,0]
	v_mfma_scale_f32_32x32x64_f8f6f4 v[50:65], v[178:185], v[210:217], v[50:65], v165, v165 op_sel_hi:[0,0,0]
	v_lshl_add_u64 v[152:153], s[38:39], 0, v[130:131]
	s_mov_b32 m0, s43
	s_nop 0
	global_load_lds_dwordx4 v[152:153], off
	v_mfma_scale_f32_32x32x64_f8f6f4 v[18:33], v[178:185], v[226:233], v[18:33], v165, v165 op_sel_hi:[0,0,0]
	v_mfma_scale_f32_32x32x64_f8f6f4 v[34:49], v[186:193], v[202:209], v[34:49], v165, v165 op_sel_hi:[0,0,0]
	v_mfma_scale_f32_32x32x64_f8f6f4 v[2:17], v[186:193], v[218:225], v[2:17], v165, v165 op_sel_hi:[0,0,0]
	s_mov_b32 m0, s44
	s_nop 0
	global_load_lds_dwordx4 v[234:235], off
	v_mfma_scale_f32_32x32x64_f8f6f4 v[34:49], v[194:201], v[210:217], v[34:49], v165, v165 op_sel_hi:[0,0,0]
	v_mfma_scale_f32_32x32x64_f8f6f4 v[2:17], v[194:201], v[226:233], v[2:17], v165, v165 op_sel_hi:[0,0,0]
	s_setprio 0
	s_barrier
	s_add_i32 s55, 0, 0x18000
	v_add_u32_e32 v138, s55, v154
	v_add_u32_e32 v174, s55, v155
	s_add_i32 s56, 0, 0x1c000
	ds_read_b128 v[170:173], v138
	ds_read_b128 v[174:177], v174
	ds_read_b128 v[178:181], v166
	ds_read_b128 v[182:185], v167
	v_add_u32_e32 v138, s56, v154
	v_add_u32_e32 v190, s56, v155
	ds_read_b128 v[186:189], v138
	ds_read_b128 v[190:193], v190
	ds_read_b128 v[194:197], v168
	ds_read_b128 v[198:201], v169
	s_add_u32 s38, s38, 0x40000
	s_addc_u32 s39, s39, 0
	s_mov_b32 m0, s45
	v_lshl_add_u64 v[236:237], s[38:39], 0, v[130:131]
	ds_read_b128 v[202:205], v163 offset:32768
	ds_read_b128 v[210:213], v163 offset:33792
	ds_read_b128 v[206:209], v164 offset:32768
	ds_read_b128 v[214:217], v164 offset:33792
	ds_read_b128 v[218:221], v163 offset:36864
	ds_read_b128 v[226:229], v163 offset:37888
	ds_read_b128 v[222:225], v164 offset:36864
	ds_read_b128 v[230:233], v164 offset:37888
	global_load_lds_dwordx4 v[236:237], off
	v_lshl_add_u64 v[236:237], s[38:39], 0, v[134:135]
	s_mov_b32 m0, s46
	s_nop 0
	global_load_lds_dwordx4 v[236:237], off
	s_waitcnt vmcnt(8)
	s_waitcnt lgkmcnt(0)
	s_barrier
	s_setprio 1
	s_waitcnt lgkmcnt(0)
	v_mfma_scale_f32_32x32x64_f8f6f4 v[114:129], v[170:177], v[202:209], v[114:129], v165, v165 op_sel_hi:[0,0,0]
	v_mfma_scale_f32_32x32x64_f8f6f4 v[82:97], v[170:177], v[218:225], v[82:97], v165, v165 op_sel_hi:[0,0,0]
	v_mfma_scale_f32_32x32x64_f8f6f4 v[114:129], v[178:185], v[210:217], v[114:129], v165, v165 op_sel_hi:[0,0,0]
	v_mfma_scale_f32_32x32x64_f8f6f4 v[82:97], v[178:185], v[226:233], v[82:97], v165, v165 op_sel_hi:[0,0,0]
	v_mfma_scale_f32_32x32x64_f8f6f4 v[98:113], v[186:193], v[202:209], v[98:113], v165, v165 op_sel_hi:[0,0,0]
	v_mfma_scale_f32_32x32x64_f8f6f4 v[66:81], v[186:193], v[218:225], v[66:81], v165, v165 op_sel_hi:[0,0,0]
	v_mfma_scale_f32_32x32x64_f8f6f4 v[98:113], v[194:201], v[210:217], v[98:113], v165, v165 op_sel_hi:[0,0,0]
	v_mfma_scale_f32_32x32x64_f8f6f4 v[66:81], v[194:201], v[226:233], v[66:81], v165, v165 op_sel_hi:[0,0,0]
	s_setprio 0
	s_barrier
	s_add_i32 s38, s55, s42
	v_lshl_add_u64 v[148:149], v[148:149], 0, s[16:17]
	s_mov_b32 m0, s38
	ds_read_b128 v[202:205], v163 offset:49152
	ds_read_b128 v[210:213], v163 offset:50176
	ds_read_b128 v[206:209], v164 offset:49152
	ds_read_b128 v[214:217], v164 offset:50176
	ds_read_b128 v[218:221], v163 offset:53248
	ds_read_b128 v[226:229], v163 offset:54272
	ds_read_b128 v[222:225], v164 offset:53248
	ds_read_b128 v[230:233], v164 offset:54272
	global_load_lds_dwordx4 v[148:149], off
	s_add_i32 m0, s38, 0x2000
	s_add_u32 s36, s36, 0x40080
	v_lshl_add_u64 v[148:149], v[150:151], 0, s[16:17]
	s_addc_u32 s37, s37, 0
	s_add_i32 s38, s56, s42
	global_load_lds_dwordx4 v[148:149], off
	v_lshl_add_u64 v[148:149], s[36:37], 0, v[132:133]
	s_mov_b32 m0, s38
	s_nop 0
	global_load_lds_dwordx4 v[148:149], off
	v_lshl_add_u64 v[148:149], s[36:37], 0, v[136:137]
	s_add_i32 m0, s38, 0x2000
	s_nop 0
	global_load_lds_dwordx4 v[148:149], off
	s_waitcnt vmcnt(6)
	s_waitcnt lgkmcnt(0)
	s_barrier
	s_setprio 1
	s_waitcnt lgkmcnt(0)
	v_mfma_scale_f32_32x32x64_f8f6f4 v[50:65], v[170:177], v[202:209], v[50:65], v165, v165 op_sel_hi:[0,0,0]
	v_mfma_scale_f32_32x32x64_f8f6f4 v[18:33], v[170:177], v[218:225], v[18:33], v165, v165 op_sel_hi:[0,0,0]
	v_mfma_scale_f32_32x32x64_f8f6f4 v[50:65], v[178:185], v[210:217], v[50:65], v165, v165 op_sel_hi:[0,0,0]
	v_lshl_add_u64 v[148:149], v[152:153], 0, s[16:17]
	s_mov_b32 m0, s47
	s_nop 0
	global_load_lds_dwordx4 v[148:149], off
	v_mfma_scale_f32_32x32x64_f8f6f4 v[18:33], v[178:185], v[226:233], v[18:33], v165, v165 op_sel_hi:[0,0,0]
	v_mfma_scale_f32_32x32x64_f8f6f4 v[34:49], v[186:193], v[202:209], v[34:49], v165, v165 op_sel_hi:[0,0,0]
	v_mfma_scale_f32_32x32x64_f8f6f4 v[2:17], v[186:193], v[218:225], v[2:17], v165, v165 op_sel_hi:[0,0,0]
	v_lshl_add_u64 v[148:149], v[234:235], 0, s[16:17]
	s_mov_b32 m0, s48
	s_nop 0
	global_load_lds_dwordx4 v[148:149], off
	v_mfma_scale_f32_32x32x64_f8f6f4 v[34:49], v[194:201], v[210:217], v[34:49], v165, v165 op_sel_hi:[0,0,0]
	v_mfma_scale_f32_32x32x64_f8f6f4 v[2:17], v[194:201], v[226:233], v[2:17], v165, v165 op_sel_hi:[0,0,0]
	s_setprio 0
	s_barrier
	s_add_i32 s29, s29, 2
	s_add_u32 s6, s6, 0x100
	s_addc_u32 s7, s7, 0
	s_add_u32 s9, s9, 0x100
	s_addc_u32 s27, s27, 0
	s_cmp_gt_u32 s29, 13
	s_cbranch_scc0 .LBB0_373
	s_and_b64 vcc, exec, s[18:19]
	s_cbranch_vccz .LBB0_376
	s_barrier

.LBB0_407:
	ds_read_b128 v[150:153], v147
	ds_read_b128 v[154:157], v147 offset:1024
	ds_read_b128 v[158:161], v147 offset:2048
	ds_read_b128 v[162:165], v147 offset:3072
	ds_read_b128 v[166:169], v148
	ds_read_b128 v[170:173], v148 offset:1024
	ds_read_b128 v[174:177], v148 offset:2048
	ds_read_b128 v[178:181], v148 offset:3072
	s_add_u32 s40, s38, 0xfff80080
	s_addc_u32 s41, s39, -1
	s_cmp_eq_u32 s68, 28
	s_cselect_b32 s43, s29, s41
	s_cselect_b32 s42, s28, s40
	s_cselect_b32 s41, s31, s37
	s_cselect_b32 s40, s30, s27
	v_lshl_add_u64 v[214:215], s[38:39], 0, v[140:141]
	s_add_i32 m0, s47, 0xc000
	ds_read_b128 v[182:185], v149
	ds_read_b128 v[186:189], v149 offset:1024
	ds_read_b128 v[190:193], v149 offset:2048
	ds_read_b128 v[194:197], v149 offset:3072
	ds_read_b128 v[198:201], v149 offset:4096
	ds_read_b128 v[202:205], v149 offset:5120
	ds_read_b128 v[206:209], v149 offset:6144
	ds_read_b128 v[210:213], v149 offset:7168
	global_load_lds_dwordx4 v[214:215], off
	v_lshl_add_u64 v[214:215], s[38:39], 0, v[142:143]
	s_add_i32 m0, s47, 0xe000
	s_nop 0
	global_load_lds_dwordx4 v[214:215], off
	s_waitcnt vmcnt(8)
	s_waitcnt lgkmcnt(0)
	s_barrier
	s_setprio 1
	s_waitcnt lgkmcnt(0)
	v_mfma_f32_16x16x32_bf16 v[126:129], v[150:153], v[182:185], v[126:129]
	v_mfma_f32_16x16x32_bf16 v[122:125], v[158:161], v[182:185], v[122:125]
	v_mfma_f32_16x16x32_bf16 v[118:121], v[150:153], v[190:193], v[118:121]
	v_mfma_f32_16x16x32_bf16 v[114:117], v[158:161], v[190:193], v[114:117]
	v_mfma_f32_16x16x32_bf16 v[110:113], v[150:153], v[198:201], v[110:113]
	v_mfma_f32_16x16x32_bf16 v[102:105], v[158:161], v[198:201], v[102:105]
	v_mfma_f32_16x16x32_bf16 v[86:89], v[150:153], v[206:209], v[86:89]
	v_mfma_f32_16x16x32_bf16 v[74:77], v[158:161], v[206:209], v[74:77]
	v_mfma_f32_16x16x32_bf16 v[126:129], v[154:157], v[186:189], v[126:129]
	v_mfma_f32_16x16x32_bf16 v[122:125], v[162:165], v[186:189], v[122:125]
	v_mfma_f32_16x16x32_bf16 v[118:121], v[154:157], v[194:197], v[118:121]
	v_mfma_f32_16x16x32_bf16 v[114:117], v[162:165], v[194:197], v[114:117]
	v_mfma_f32_16x16x32_bf16 v[110:113], v[154:157], v[202:205], v[110:113]
	v_mfma_f32_16x16x32_bf16 v[102:105], v[162:165], v[202:205], v[102:105]
	v_mfma_f32_16x16x32_bf16 v[86:89], v[154:157], v[210:213], v[86:89]
	v_mfma_f32_16x16x32_bf16 v[74:77], v[162:165], v[210:213], v[74:77]
	v_mfma_f32_16x16x32_bf16 v[106:109], v[166:169], v[182:185], v[106:109]
	v_mfma_f32_16x16x32_bf16 v[98:101], v[174:177], v[182:185], v[98:101]
	v_mfma_f32_16x16x32_bf16 v[94:97], v[166:169], v[190:193], v[94:97]
	v_mfma_f32_16x16x32_bf16 v[90:93], v[174:177], v[190:193], v[90:93]
	v_mfma_f32_16x16x32_bf16 v[82:85], v[166:169], v[198:201], v[82:85]
	v_mfma_f32_16x16x32_bf16 v[78:81], v[174:177], v[198:201], v[78:81]
	v_mfma_f32_16x16x32_bf16 v[70:73], v[166:169], v[206:209], v[70:73]
	v_mfma_f32_16x16x32_bf16 v[66:69], v[174:177], v[206:209], v[66:69]
	v_mfma_f32_16x16x32_bf16 v[106:109], v[170:173], v[186:189], v[106:109]
	v_mfma_f32_16x16x32_bf16 v[98:101], v[178:181], v[186:189], v[98:101]
	v_mfma_f32_16x16x32_bf16 v[94:97], v[170:173], v[194:197], v[94:97]
	v_mfma_f32_16x16x32_bf16 v[90:93], v[178:181], v[194:197], v[90:93]
	v_mfma_f32_16x16x32_bf16 v[82:85], v[170:173], v[202:205], v[82:85]
	v_mfma_f32_16x16x32_bf16 v[78:81], v[178:181], v[202:205], v[78:81]
	v_mfma_f32_16x16x32_bf16 v[70:73], v[170:173], v[210:213], v[70:73]
	v_mfma_f32_16x16x32_bf16 v[66:69], v[178:181], v[210:213], v[66:69]
	s_setprio 0
	s_barrier
	s_add_i32 s69, s57, s3
	v_lshl_add_u64 v[214:215], s[40:41], 0, v[134:135]
	s_mov_b32 m0, s69
	ds_read_b128 v[182:185], v149 offset:16384
	ds_read_b128 v[186:189], v149 offset:17408
	ds_read_b128 v[190:193], v149 offset:18432
	ds_read_b128 v[194:197], v149 offset:19456
	ds_read_b128 v[198:201], v149 offset:20480
	ds_read_b128 v[202:205], v149 offset:21504
	ds_read_b128 v[206:209], v149 offset:22528
	ds_read_b128 v[210:213], v149 offset:23552
	global_load_lds_dwordx4 v[214:215], off
	s_add_i32 m0, s69, 0x2000
	s_add_u32 s70, s40, 0x80000
	v_lshl_add_u64 v[216:217], s[40:41], 0, v[130:131]
	s_addc_u32 s71, s41, 0
	s_add_i32 s69, s58, s3
	global_load_lds_dwordx4 v[216:217], off
	v_lshl_add_u64 v[218:219], s[70:71], 0, v[134:135]
	s_mov_b32 m0, s69
	v_lshl_add_u64 v[220:221], s[42:43], 0, v[132:133]
	global_load_lds_dwordx4 v[218:219], off
	v_lshl_add_u64 v[218:219], s[70:71], 0, v[130:131]
	s_add_i32 m0, s69, 0x2000
	s_nop 0
	global_load_lds_dwordx4 v[218:219], off
	s_waitcnt vmcnt(6)
	s_waitcnt lgkmcnt(0)
	s_barrier
	s_setprio 1
	s_waitcnt lgkmcnt(0)
	v_mfma_f32_16x16x32_bf16 v[62:65], v[150:153], v[182:185], v[62:65]
	v_mfma_f32_16x16x32_bf16 v[58:61], v[158:161], v[182:185], v[58:61]
	v_mfma_f32_16x16x32_bf16 v[54:57], v[150:153], v[190:193], v[54:57]
	v_mfma_f32_16x16x32_bf16 v[46:49], v[158:161], v[190:193], v[46:49]
	v_mfma_f32_16x16x32_bf16 v[38:41], v[150:153], v[198:201], v[38:41]
	v_mfma_f32_16x16x32_bf16 v[30:33], v[158:161], v[198:201], v[30:33]
	v_mfma_f32_16x16x32_bf16 v[22:25], v[150:153], v[206:209], v[22:25]
	v_mfma_f32_16x16x32_bf16 v[14:17], v[158:161], v[206:209], v[14:17]
	v_mfma_f32_16x16x32_bf16 v[62:65], v[154:157], v[186:189], v[62:65]
	v_lshl_add_u64 v[218:219], s[42:43], 0, v[136:137]
	s_mov_b32 m0, s47
	s_nop 0
	global_load_lds_dwordx4 v[218:219], off
	v_mfma_f32_16x16x32_bf16 v[58:61], v[162:165], v[186:189], v[58:61]
	v_mfma_f32_16x16x32_bf16 v[54:57], v[154:157], v[194:197], v[54:57]
	v_mfma_f32_16x16x32_bf16 v[46:49], v[162:165], v[194:197], v[46:49]
	v_mfma_f32_16x16x32_bf16 v[38:41], v[154:157], v[202:205], v[38:41]
	v_mfma_f32_16x16x32_bf16 v[30:33], v[162:165], v[202:205], v[30:33]
	v_mfma_f32_16x16x32_bf16 v[22:25], v[154:157], v[210:213], v[22:25]
	v_mfma_f32_16x16x32_bf16 v[14:17], v[162:165], v[210:213], v[14:17]
	v_mfma_f32_16x16x32_bf16 v[50:53], v[166:169], v[182:185], v[50:53]
	v_mfma_f32_16x16x32_bf16 v[42:45], v[174:177], v[182:185], v[42:45]
	v_mfma_f32_16x16x32_bf16 v[34:37], v[166:169], v[190:193], v[34:37]
	v_mfma_f32_16x16x32_bf16 v[26:29], v[174:177], v[190:193], v[26:29]
	v_mfma_f32_16x16x32_bf16 v[18:21], v[166:169], v[198:201], v[18:21]
	s_mov_b32 m0, s48
	s_nop 0
	global_load_lds_dwordx4 v[220:221], off
	v_mfma_f32_16x16x32_bf16 v[10:13], v[174:177], v[198:201], v[10:13]
	v_mfma_f32_16x16x32_bf16 v[6:9], v[166:169], v[206:209], v[6:9]
	v_mfma_f32_16x16x32_bf16 v[2:5], v[174:177], v[206:209], v[2:5]
	v_mfma_f32_16x16x32_bf16 v[50:53], v[170:173], v[186:189], v[50:53]
	v_mfma_f32_16x16x32_bf16 v[42:45], v[178:181], v[186:189], v[42:45]
	v_mfma_f32_16x16x32_bf16 v[34:37], v[170:173], v[194:197], v[34:37]
	v_mfma_f32_16x16x32_bf16 v[26:29], v[178:181], v[194:197], v[26:29]
	v_mfma_f32_16x16x32_bf16 v[18:21], v[170:173], v[202:205], v[18:21]
	v_mfma_f32_16x16x32_bf16 v[10:13], v[178:181], v[202:205], v[10:13]
	v_mfma_f32_16x16x32_bf16 v[6:9], v[170:173], v[210:213], v[6:9]
	v_mfma_f32_16x16x32_bf16 v[2:5], v[178:181], v[210:213], v[2:5]
	s_setprio 0
	s_barrier
	s_add_i32 s69, 0, 0x18000
	v_add_u32_e32 v138, s69, v145
	s_add_i32 s70, 0, 0x1c000
	ds_read_b128 v[150:153], v138
	ds_read_b128 v[154:157], v138 offset:1024
	ds_read_b128 v[158:161], v138 offset:2048
	ds_read_b128 v[162:165], v138 offset:3072
	v_add_u32_e32 v138, s70, v145
	ds_read_b128 v[166:169], v138
	ds_read_b128 v[170:173], v138 offset:1024
	ds_read_b128 v[174:177], v138 offset:2048
	ds_read_b128 v[178:181], v138 offset:3072
	s_add_u32 s42, s42, 0x80000
	s_addc_u32 s43, s43, 0
	s_mov_b32 m0, s49
	v_lshl_add_u64 v[222:223], s[42:43], 0, v[136:137]
	ds_read_b128 v[182:185], v149 offset:32768
	ds_read_b128 v[186:189], v149 offset:33792
	ds_read_b128 v[190:193], v149 offset:34816
	ds_read_b128 v[194:197], v149 offset:35840
	ds_read_b128 v[198:201], v149 offset:36864
	ds_read_b128 v[202:205], v149 offset:37888
	ds_read_b128 v[206:209], v149 offset:38912
	ds_read_b128 v[210:213], v149 offset:39936
	global_load_lds_dwordx4 v[222:223], off
	v_lshl_add_u64 v[222:223], s[42:43], 0, v[132:133]
	s_mov_b32 m0, s50
	s_nop 0
	global_load_lds_dwordx4 v[222:223], off
	s_waitcnt vmcnt(8)
	s_waitcnt lgkmcnt(0)
	s_barrier
	s_setprio 1
	s_waitcnt lgkmcnt(0)
	v_mfma_f32_16x16x32_bf16 v[126:129], v[150:153], v[182:185], v[126:129]
	v_mfma_f32_16x16x32_bf16 v[122:125], v[158:161], v[182:185], v[122:125]
	v_mfma_f32_16x16x32_bf16 v[118:121], v[150:153], v[190:193], v[118:121]
	v_mfma_f32_16x16x32_bf16 v[114:117], v[158:161], v[190:193], v[114:117]
	v_mfma_f32_16x16x32_bf16 v[110:113], v[150:153], v[198:201], v[110:113]
	v_mfma_f32_16x16x32_bf16 v[102:105], v[158:161], v[198:201], v[102:105]
	v_mfma_f32_16x16x32_bf16 v[86:89], v[150:153], v[206:209], v[86:89]
	v_mfma_f32_16x16x32_bf16 v[74:77], v[158:161], v[206:209], v[74:77]
	v_mfma_f32_16x16x32_bf16 v[126:129], v[154:157], v[186:189], v[126:129]
	v_mfma_f32_16x16x32_bf16 v[122:125], v[162:165], v[186:189], v[122:125]
	v_mfma_f32_16x16x32_bf16 v[118:121], v[154:157], v[194:197], v[118:121]
	v_mfma_f32_16x16x32_bf16 v[114:117], v[162:165], v[194:197], v[114:117]
	v_mfma_f32_16x16x32_bf16 v[110:113], v[154:157], v[202:205], v[110:113]
	v_mfma_f32_16x16x32_bf16 v[102:105], v[162:165], v[202:205], v[102:105]
	v_mfma_f32_16x16x32_bf16 v[86:89], v[154:157], v[210:213], v[86:89]
	v_mfma_f32_16x16x32_bf16 v[74:77], v[162:165], v[210:213], v[74:77]
	v_mfma_f32_16x16x32_bf16 v[106:109], v[166:169], v[182:185], v[106:109]
	v_mfma_f32_16x16x32_bf16 v[98:101], v[174:177], v[182:185], v[98:101]
	v_mfma_f32_16x16x32_bf16 v[94:97], v[166:169], v[190:193], v[94:97]
	v_mfma_f32_16x16x32_bf16 v[90:93], v[174:177], v[190:193], v[90:93]
	v_mfma_f32_16x16x32_bf16 v[82:85], v[166:169], v[198:201], v[82:85]
	v_mfma_f32_16x16x32_bf16 v[78:81], v[174:177], v[198:201], v[78:81]
	v_mfma_f32_16x16x32_bf16 v[70:73], v[166:169], v[206:209], v[70:73]
	v_mfma_f32_16x16x32_bf16 v[66:69], v[174:177], v[206:209], v[66:69]
	v_mfma_f32_16x16x32_bf16 v[106:109], v[170:173], v[186:189], v[106:109]
	v_mfma_f32_16x16x32_bf16 v[98:101], v[178:181], v[186:189], v[98:101]
	v_mfma_f32_16x16x32_bf16 v[94:97], v[170:173], v[194:197], v[94:97]
	v_mfma_f32_16x16x32_bf16 v[90:93], v[178:181], v[194:197], v[90:93]
	v_mfma_f32_16x16x32_bf16 v[82:85], v[170:173], v[202:205], v[82:85]
	v_mfma_f32_16x16x32_bf16 v[78:81], v[178:181], v[202:205], v[78:81]
	v_mfma_f32_16x16x32_bf16 v[70:73], v[170:173], v[210:213], v[70:73]
	v_mfma_f32_16x16x32_bf16 v[66:69], v[178:181], v[210:213], v[66:69]
	s_setprio 0
	s_barrier
	s_add_i32 s42, s69, s3
	v_lshl_add_u64 v[214:215], v[214:215], 0, s[16:17]
	s_mov_b32 m0, s42
	ds_read_b128 v[182:185], v149 offset:49152
	ds_read_b128 v[186:189], v149 offset:50176
	ds_read_b128 v[190:193], v149 offset:51200
	ds_read_b128 v[194:197], v149 offset:52224
	ds_read_b128 v[198:201], v149 offset:53248
	ds_read_b128 v[202:205], v149 offset:54272
	ds_read_b128 v[206:209], v149 offset:55296
	ds_read_b128 v[210:213], v149 offset:56320
	global_load_lds_dwordx4 v[214:215], off
	s_add_i32 m0, s42, 0x2000
	s_add_u32 s40, s40, 0x80080
	v_lshl_add_u64 v[214:215], v[216:217], 0, s[16:17]
	s_addc_u32 s41, s41, 0
	s_add_i32 s42, s70, s3
	global_load_lds_dwordx4 v[214:215], off
	v_lshl_add_u64 v[214:215], s[40:41], 0, v[134:135]
	s_mov_b32 m0, s42
	s_nop 0
	global_load_lds_dwordx4 v[214:215], off
	v_lshl_add_u64 v[214:215], s[40:41], 0, v[130:131]
	s_add_i32 m0, s42, 0x2000
	s_nop 0
	global_load_lds_dwordx4 v[214:215], off
	s_waitcnt vmcnt(6)
	s_waitcnt lgkmcnt(0)
	s_barrier
	s_setprio 1
	s_waitcnt lgkmcnt(0)
	v_mfma_f32_16x16x32_bf16 v[62:65], v[150:153], v[182:185], v[62:65]
	v_mfma_f32_16x16x32_bf16 v[58:61], v[158:161], v[182:185], v[58:61]
	v_mfma_f32_16x16x32_bf16 v[54:57], v[150:153], v[190:193], v[54:57]
	v_mfma_f32_16x16x32_bf16 v[46:49], v[158:161], v[190:193], v[46:49]
	v_mfma_f32_16x16x32_bf16 v[38:41], v[150:153], v[198:201], v[38:41]
	v_mfma_f32_16x16x32_bf16 v[30:33], v[158:161], v[198:201], v[30:33]
	v_mfma_f32_16x16x32_bf16 v[22:25], v[150:153], v[206:209], v[22:25]
	v_mfma_f32_16x16x32_bf16 v[14:17], v[158:161], v[206:209], v[14:17]
	v_mfma_f32_16x16x32_bf16 v[62:65], v[154:157], v[186:189], v[62:65]
	v_lshl_add_u64 v[214:215], v[218:219], 0, s[16:17]
	s_mov_b32 m0, s55
	s_nop 0
	global_load_lds_dwordx4 v[214:215], off
	v_mfma_f32_16x16x32_bf16 v[58:61], v[162:165], v[186:189], v[58:61]
	v_mfma_f32_16x16x32_bf16 v[54:57], v[154:157], v[194:197], v[54:57]
	v_mfma_f32_16x16x32_bf16 v[46:49], v[162:165], v[194:197], v[46:49]
	v_mfma_f32_16x16x32_bf16 v[38:41], v[154:157], v[202:205], v[38:41]
	v_mfma_f32_16x16x32_bf16 v[30:33], v[162:165], v[202:205], v[30:33]
	v_mfma_f32_16x16x32_bf16 v[22:25], v[154:157], v[210:213], v[22:25]
	v_mfma_f32_16x16x32_bf16 v[14:17], v[162:165], v[210:213], v[14:17]
	v_mfma_f32_16x16x32_bf16 v[50:53], v[166:169], v[182:185], v[50:53]
	v_mfma_f32_16x16x32_bf16 v[42:45], v[174:177], v[182:185], v[42:45]
	v_mfma_f32_16x16x32_bf16 v[34:37], v[166:169], v[190:193], v[34:37]
	v_mfma_f32_16x16x32_bf16 v[26:29], v[174:177], v[190:193], v[26:29]
	v_mfma_f32_16x16x32_bf16 v[18:21], v[166:169], v[198:201], v[18:21]
	v_lshl_add_u64 v[214:215], v[220:221], 0, s[16:17]
	s_mov_b32 m0, s56
	s_nop 0
	global_load_lds_dwordx4 v[214:215], off
	v_mfma_f32_16x16x32_bf16 v[10:13], v[174:177], v[198:201], v[10:13]
	v_mfma_f32_16x16x32_bf16 v[6:9], v[166:169], v[206:209], v[6:9]
	v_mfma_f32_16x16x32_bf16 v[2:5], v[174:177], v[206:209], v[2:5]
	v_mfma_f32_16x16x32_bf16 v[50:53], v[170:173], v[186:189], v[50:53]
	v_mfma_f32_16x16x32_bf16 v[42:45], v[178:181], v[186:189], v[42:45]
	v_mfma_f32_16x16x32_bf16 v[34:37], v[170:173], v[194:197], v[34:37]
	v_mfma_f32_16x16x32_bf16 v[26:29], v[178:181], v[194:197], v[26:29]
	v_mfma_f32_16x16x32_bf16 v[18:21], v[170:173], v[202:205], v[18:21]
	v_mfma_f32_16x16x32_bf16 v[10:13], v[178:181], v[202:205], v[10:13]
	v_mfma_f32_16x16x32_bf16 v[6:9], v[170:173], v[210:213], v[6:9]
	v_mfma_f32_16x16x32_bf16 v[2:5], v[178:181], v[210:213], v[2:5]
	s_setprio 0
	s_barrier
	s_add_i32 s68, s68, 2
	s_add_u32 s38, s38, 0x100
	s_addc_u32 s39, s39, 0
	s_add_u32 s27, s27, 0x100
	s_addc_u32 s37, s37, 0
	s_cmp_gt_u32 s68, 29
	s_cbranch_scc0 .LBB0_407
	s_and_b64 vcc, exec, s[18:19]
	s_cbranch_vccz .LBB0_410
	s_barrier

.LBB0_769:
	ds_read_b128 v[130:133], v159
	ds_read_b128 v[134:137], v160
	ds_read_b128 v[174:177], v161
	ds_read_b128 v[178:181], v162
	ds_read_b128 v[182:185], v163
	ds_read_b128 v[186:189], v164
	ds_read_b128 v[190:193], v165
	ds_read_b128 v[194:197], v166
	s_add_u32 s44, s42, 0xfffc0080
	s_addc_u32 s45, s43, -1
	s_cmp_eq_u32 s41, 12
	s_cselect_b32 s47, s37, s45
	s_cselect_b32 s46, s36, s44
	s_cselect_b32 s45, s39, s35
	s_cselect_b32 s44, s38, s31
	v_lshl_add_u64 v[154:155], s[42:43], 0, v[146:147]
	s_add_i32 m0, s51, 0xc000
	ds_read_b128 v[198:201], v167
	ds_read_b128 v[206:209], v167 offset:1024
	ds_read_b128 v[202:205], v168
	ds_read_b128 v[210:213], v168 offset:1024
	ds_read_b128 v[214:217], v167 offset:4096
	ds_read_b128 v[222:225], v167 offset:5120
	ds_read_b128 v[218:221], v168 offset:4096
	ds_read_b128 v[226:229], v168 offset:5120
	global_load_lds_dwordx4 v[154:155], off
	v_lshl_add_u64 v[154:155], s[42:43], 0, v[148:149]
	s_add_i32 m0, s51, 0xe000
	s_nop 0
	global_load_lds_dwordx4 v[154:155], off
	s_waitcnt vmcnt(8)
	s_waitcnt lgkmcnt(0)
	s_barrier
	s_setprio 1
	s_waitcnt lgkmcnt(0)
	v_mfma_scale_f32_32x32x64_f8f6f4 v[114:129], v[130:137], v[198:205], v[114:129], v169, v169 op_sel_hi:[0,0,0]
	v_mfma_scale_f32_32x32x64_f8f6f4 v[82:97], v[130:137], v[214:221], v[82:97], v169, v169 op_sel_hi:[0,0,0]
	v_mfma_scale_f32_32x32x64_f8f6f4 v[114:129], v[174:181], v[206:213], v[114:129], v169, v169 op_sel_hi:[0,0,0]
	v_mfma_scale_f32_32x32x64_f8f6f4 v[82:97], v[174:181], v[222:229], v[82:97], v169, v169 op_sel_hi:[0,0,0]
	v_mfma_scale_f32_32x32x64_f8f6f4 v[98:113], v[182:189], v[198:205], v[98:113], v169, v169 op_sel_hi:[0,0,0]
	v_mfma_scale_f32_32x32x64_f8f6f4 v[66:81], v[182:189], v[214:221], v[66:81], v169, v169 op_sel_hi:[0,0,0]
	v_mfma_scale_f32_32x32x64_f8f6f4 v[98:113], v[190:197], v[206:213], v[98:113], v169, v169 op_sel_hi:[0,0,0]
	v_mfma_scale_f32_32x32x64_f8f6f4 v[66:81], v[190:197], v[222:229], v[66:81], v169, v169 op_sel_hi:[0,0,0]
	s_setprio 0
	s_barrier
	s_add_i32 s65, s59, s50
	v_lshl_add_u64 v[154:155], s[44:45], 0, v[140:141]
	s_mov_b32 m0, s65
	ds_read_b128 v[198:201], v167 offset:16384
	ds_read_b128 v[206:209], v167 offset:17408
	ds_read_b128 v[202:205], v168 offset:16384
	ds_read_b128 v[210:213], v168 offset:17408
	ds_read_b128 v[214:217], v167 offset:20480
	ds_read_b128 v[222:225], v167 offset:21504
	ds_read_b128 v[218:221], v168 offset:20480
	ds_read_b128 v[226:229], v168 offset:21504
	global_load_lds_dwordx4 v[154:155], off
	s_add_i32 m0, s65, 0x2000
	s_add_u32 s66, s44, 0x40000
	v_lshl_add_u64 v[156:157], s[44:45], 0, v[144:145]
	s_addc_u32 s67, s45, 0
	s_add_i32 s65, s60, s50
	global_load_lds_dwordx4 v[156:157], off
	v_lshl_add_u64 v[230:231], s[66:67], 0, v[140:141]
	s_mov_b32 m0, s65
	v_lshl_add_u64 v[232:233], s[46:47], 0, v[142:143]
	global_load_lds_dwordx4 v[230:231], off
	v_lshl_add_u64 v[230:231], s[66:67], 0, v[144:145]
	s_add_i32 m0, s65, 0x2000
	s_nop 0
	global_load_lds_dwordx4 v[230:231], off
	s_waitcnt vmcnt(6)
	s_waitcnt lgkmcnt(0)
	s_barrier
	s_setprio 1
	s_waitcnt lgkmcnt(0)
	v_mfma_scale_f32_32x32x64_f8f6f4 v[50:65], v[130:137], v[198:205], v[50:65], v169, v169 op_sel_hi:[0,0,0]
	v_mfma_scale_f32_32x32x64_f8f6f4 v[18:33], v[130:137], v[214:221], v[18:33], v169, v169 op_sel_hi:[0,0,0]
	v_mfma_scale_f32_32x32x64_f8f6f4 v[50:65], v[174:181], v[206:213], v[50:65], v169, v169 op_sel_hi:[0,0,0]
	v_lshl_add_u64 v[230:231], s[46:47], 0, v[138:139]
	s_mov_b32 m0, s51
	s_nop 0
	global_load_lds_dwordx4 v[230:231], off
	v_mfma_scale_f32_32x32x64_f8f6f4 v[18:33], v[174:181], v[222:229], v[18:33], v169, v169 op_sel_hi:[0,0,0]
	v_mfma_scale_f32_32x32x64_f8f6f4 v[34:49], v[182:189], v[198:205], v[34:49], v169, v169 op_sel_hi:[0,0,0]
	v_mfma_scale_f32_32x32x64_f8f6f4 v[2:17], v[182:189], v[214:221], v[2:17], v169, v169 op_sel_hi:[0,0,0]
	s_mov_b32 m0, s52
	s_nop 0
	global_load_lds_dwordx4 v[232:233], off
	v_mfma_scale_f32_32x32x64_f8f6f4 v[34:49], v[190:197], v[206:213], v[34:49], v169, v169 op_sel_hi:[0,0,0]
	v_mfma_scale_f32_32x32x64_f8f6f4 v[2:17], v[190:197], v[222:229], v[2:17], v169, v169 op_sel_hi:[0,0,0]
	s_setprio 0
	s_barrier
	s_add_i32 s65, 0, 0x18000
	s_add_i32 s66, 0, 0x1c000
	v_add_u32_e32 v130, s65, v1
	v_add_u32_e32 v134, s65, v158
	v_add_u32_e32 v182, s66, v1
	v_add_u32_e32 v186, s66, v158
	ds_read_b128 v[130:133], v130
	ds_read_b128 v[134:137], v134
	ds_read_b128 v[174:177], v170
	ds_read_b128 v[178:181], v171
	ds_read_b128 v[182:185], v182
	ds_read_b128 v[186:189], v186
	ds_read_b128 v[190:193], v172
	ds_read_b128 v[194:197], v173
	s_add_u32 s46, s46, 0x40000
	s_addc_u32 s47, s47, 0
	s_mov_b32 m0, s53
	v_lshl_add_u64 v[234:235], s[46:47], 0, v[138:139]
	ds_read_b128 v[198:201], v167 offset:32768
	ds_read_b128 v[206:209], v167 offset:33792
	ds_read_b128 v[202:205], v168 offset:32768
	ds_read_b128 v[210:213], v168 offset:33792
	ds_read_b128 v[214:217], v167 offset:36864
	ds_read_b128 v[222:225], v167 offset:37888
	ds_read_b128 v[218:221], v168 offset:36864
	ds_read_b128 v[226:229], v168 offset:37888
	global_load_lds_dwordx4 v[234:235], off
	v_lshl_add_u64 v[234:235], s[46:47], 0, v[142:143]
	s_mov_b32 m0, s54
	s_nop 0
	global_load_lds_dwordx4 v[234:235], off
	s_waitcnt vmcnt(8)
	s_waitcnt lgkmcnt(0)
	s_barrier
	s_setprio 1
	s_waitcnt lgkmcnt(0)
	v_mfma_scale_f32_32x32x64_f8f6f4 v[114:129], v[130:137], v[198:205], v[114:129], v169, v169 op_sel_hi:[0,0,0]
	v_mfma_scale_f32_32x32x64_f8f6f4 v[82:97], v[130:137], v[214:221], v[82:97], v169, v169 op_sel_hi:[0,0,0]
	v_mfma_scale_f32_32x32x64_f8f6f4 v[114:129], v[174:181], v[206:213], v[114:129], v169, v169 op_sel_hi:[0,0,0]
	v_mfma_scale_f32_32x32x64_f8f6f4 v[82:97], v[174:181], v[222:229], v[82:97], v169, v169 op_sel_hi:[0,0,0]
	v_mfma_scale_f32_32x32x64_f8f6f4 v[98:113], v[182:189], v[198:205], v[98:113], v169, v169 op_sel_hi:[0,0,0]
	v_mfma_scale_f32_32x32x64_f8f6f4 v[66:81], v[182:189], v[214:221], v[66:81], v169, v169 op_sel_hi:[0,0,0]
	v_mfma_scale_f32_32x32x64_f8f6f4 v[98:113], v[190:197], v[206:213], v[98:113], v169, v169 op_sel_hi:[0,0,0]
	v_mfma_scale_f32_32x32x64_f8f6f4 v[66:81], v[190:197], v[222:229], v[66:81], v169, v169 op_sel_hi:[0,0,0]
	s_setprio 0
	s_barrier
	s_add_i32 s46, s65, s50
	v_lshl_add_u64 v[154:155], v[154:155], 0, s[14:15]
	s_mov_b32 m0, s46
	ds_read_b128 v[198:201], v167 offset:49152
	ds_read_b128 v[206:209], v167 offset:50176
	ds_read_b128 v[202:205], v168 offset:49152
	ds_read_b128 v[210:213], v168 offset:50176
	ds_read_b128 v[214:217], v167 offset:53248
	ds_read_b128 v[222:225], v167 offset:54272
	ds_read_b128 v[218:221], v168 offset:53248
	ds_read_b128 v[226:229], v168 offset:54272
	global_load_lds_dwordx4 v[154:155], off
	s_add_i32 m0, s46, 0x2000
	s_add_u32 s44, s44, 0x40080
	v_lshl_add_u64 v[154:155], v[156:157], 0, s[14:15]
	s_addc_u32 s45, s45, 0
	s_add_i32 s46, s66, s50
	global_load_lds_dwordx4 v[154:155], off
	v_lshl_add_u64 v[154:155], s[44:45], 0, v[140:141]
	s_mov_b32 m0, s46
	s_nop 0
	global_load_lds_dwordx4 v[154:155], off
	v_lshl_add_u64 v[154:155], s[44:45], 0, v[144:145]
	s_add_i32 m0, s46, 0x2000
	s_nop 0
	global_load_lds_dwordx4 v[154:155], off
	s_waitcnt vmcnt(6)
	s_waitcnt lgkmcnt(0)
	s_barrier
	s_setprio 1
	s_waitcnt lgkmcnt(0)
	v_mfma_scale_f32_32x32x64_f8f6f4 v[50:65], v[130:137], v[198:205], v[50:65], v169, v169 op_sel_hi:[0,0,0]
	v_mfma_scale_f32_32x32x64_f8f6f4 v[18:33], v[130:137], v[214:221], v[18:33], v169, v169 op_sel_hi:[0,0,0]
	v_mfma_scale_f32_32x32x64_f8f6f4 v[50:65], v[174:181], v[206:213], v[50:65], v169, v169 op_sel_hi:[0,0,0]
	v_lshl_add_u64 v[154:155], v[230:231], 0, s[14:15]
	s_mov_b32 m0, s56
	s_nop 0
	global_load_lds_dwordx4 v[154:155], off
	v_mfma_scale_f32_32x32x64_f8f6f4 v[18:33], v[174:181], v[222:229], v[18:33], v169, v169 op_sel_hi:[0,0,0]
	v_mfma_scale_f32_32x32x64_f8f6f4 v[34:49], v[182:189], v[198:205], v[34:49], v169, v169 op_sel_hi:[0,0,0]
	v_mfma_scale_f32_32x32x64_f8f6f4 v[2:17], v[182:189], v[214:221], v[2:17], v169, v169 op_sel_hi:[0,0,0]
	v_lshl_add_u64 v[154:155], v[232:233], 0, s[14:15]
	s_mov_b32 m0, s57
	s_nop 0
	global_load_lds_dwordx4 v[154:155], off
	v_mfma_scale_f32_32x32x64_f8f6f4 v[34:49], v[190:197], v[206:213], v[34:49], v169, v169 op_sel_hi:[0,0,0]
	v_mfma_scale_f32_32x32x64_f8f6f4 v[2:17], v[190:197], v[222:229], v[2:17], v169, v169 op_sel_hi:[0,0,0]
	s_setprio 0
	s_barrier
	s_add_i32 s41, s41, 2
	s_add_u32 s42, s42, 0x100
	s_addc_u32 s43, s43, 0
	s_add_u32 s31, s31, 0x100
	s_addc_u32 s35, s35, 0
	s_cmp_gt_u32 s41, 13
	s_cbranch_scc0 .LBB0_769
	s_and_b64 vcc, exec, s[16:17]
	s_cbranch_vccz .LBB0_772
	s_barrier

.LBB0_925:
	s_waitcnt vmcnt(8)
	s_add_u32 s36, s30, 0x80
	s_waitcnt lgkmcnt(0)
	s_addc_u32 s37, s31, 0
	s_and_b64 s[34:35], s[34:35], exec
	v_mov_b32_e32 v205, v199
	s_cselect_b32 s37, s11, s37
	s_cselect_b32 s36, s10, s36
	s_cselect_b32 s35, s23, s27
	s_cselect_b32 s34, s22, s25
	s_barrier
	s_setprio 1
	s_waitcnt lgkmcnt(0)
	v_mfma_scale_f32_32x32x64_f8f6f4 v[114:129], v[154:161], v[178:185], v[114:129], v224, v224 op_sel_hi:[0,0,0]
	v_mfma_scale_f32_32x32x64_f8f6f4 v[82:97], v[154:161], v[186:193], v[82:97], v224, v224 op_sel_hi:[0,0,0]
	v_mfma_scale_f32_32x32x64_f8f6f4 v[114:129], v[146:153], v[162:169], v[114:129], v224, v224 op_sel_hi:[0,0,0]
	v_mfma_scale_f32_32x32x64_f8f6f4 v[82:97], v[146:153], v[170:177], v[82:97], v224, v224 op_sel_hi:[0,0,0]
	v_mfma_scale_f32_32x32x64_f8f6f4 v[98:113], v[138:145], v[178:185], v[98:113], v224, v224 op_sel_hi:[0,0,0]
	v_mfma_scale_f32_32x32x64_f8f6f4 v[66:81], v[138:145], v[186:193], v[66:81], v224, v224 op_sel_hi:[0,0,0]
	v_mfma_scale_f32_32x32x64_f8f6f4 v[98:113], v[130:137], v[162:169], v[98:113], v224, v224 op_sel_hi:[0,0,0]
	v_mfma_scale_f32_32x32x64_f8f6f4 v[66:81], v[130:137], v[170:177], v[66:81], v224, v224 op_sel_hi:[0,0,0]
	s_setprio 0
	s_barrier
	s_mov_b32 m0, s42
	v_lshl_add_u64 v[232:233], s[34:35], 0, v[194:195]
	s_add_u32 s66, s34, 0x40000
	ds_read_b128 v[162:165], v221 offset:16384
	ds_read_b128 v[170:173], v221 offset:17408
	ds_read_b128 v[166:169], v223 offset:16384
	ds_read_b128 v[174:177], v223 offset:17408
	ds_read_b128 v[178:181], v221 offset:20480
	ds_read_b128 v[186:189], v221 offset:21504
	ds_read_b128 v[182:185], v223 offset:20480
	ds_read_b128 v[190:193], v223 offset:21504
	global_load_lds_dwordx4 v[232:233], off
	v_lshl_add_u64 v[234:235], s[34:35], 0, v[196:197]
	s_mov_b32 m0, s43
	s_addc_u32 s67, s35, 0
	global_load_lds_dwordx4 v[234:235], off
	v_lshl_add_u64 v[236:237], s[66:67], 0, v[194:195]
	s_mov_b32 m0, s44
	v_mov_b32_e32 v203, v199
	global_load_lds_dwordx4 v[236:237], off
	v_lshl_add_u64 v[236:237], s[66:67], 0, v[196:197]
	s_mov_b32 m0, s45
	v_lshl_add_u64 v[238:239], s[36:37], 0, v[202:203]
	global_load_lds_dwordx4 v[236:237], off
	s_waitcnt vmcnt(6)
	s_waitcnt lgkmcnt(0)
	s_barrier
	s_setprio 1
	s_waitcnt lgkmcnt(0)
	v_mfma_scale_f32_32x32x64_f8f6f4 v[50:65], v[154:161], v[162:169], v[50:65], v224, v224 op_sel_hi:[0,0,0]
	v_mfma_scale_f32_32x32x64_f8f6f4 v[18:33], v[154:161], v[178:185], v[18:33], v224, v224 op_sel_hi:[0,0,0]
	v_mfma_scale_f32_32x32x64_f8f6f4 v[50:65], v[146:153], v[170:177], v[50:65], v224, v224 op_sel_hi:[0,0,0]
	s_mov_b32 m0, s41
	v_lshl_add_u64 v[236:237], s[36:37], 0, v[198:199]
	global_load_lds_dwordx4 v198, s[36:37]
	v_mfma_scale_f32_32x32x64_f8f6f4 v[18:33], v[146:153], v[186:193], v[18:33], v224, v224 op_sel_hi:[0,0,0]
	v_mfma_scale_f32_32x32x64_f8f6f4 v[34:49], v[138:145], v[162:169], v[34:49], v224, v224 op_sel_hi:[0,0,0]
	v_mfma_scale_f32_32x32x64_f8f6f4 v[2:17], v[138:145], v[178:185], v[2:17], v224, v224 op_sel_hi:[0,0,0]
	s_mov_b32 m0, s46
	s_nop 0
	global_load_lds_dwordx4 v202, s[36:37]
	v_mfma_scale_f32_32x32x64_f8f6f4 v[34:49], v[130:137], v[170:177], v[34:49], v224, v224 op_sel_hi:[0,0,0]
	v_mfma_scale_f32_32x32x64_f8f6f4 v[2:17], v[130:137], v[186:193], v[2:17], v224, v224 op_sel_hi:[0,0,0]
	s_setprio 0
	s_barrier
	s_add_i32 s65, 0, 0x18000
	s_add_i32 s66, 0, 0x1c000
	v_add_u32_e32 v130, s65, v210
	v_add_u32_e32 v134, s65, v211
	v_add_u32_e32 v138, s57, v210
	v_add_u32_e32 v142, s57, v211
	v_add_u32_e32 v146, s66, v210
	v_add_u32_e32 v150, s66, v211
	v_add_u32_e32 v154, s58, v210
	v_add_u32_e32 v158, s58, v211
	ds_read_b128 v[130:133], v130
	ds_read_b128 v[134:137], v134
	ds_read_b128 v[138:141], v138
	ds_read_b128 v[142:145], v142
	ds_read_b128 v[146:149], v146
	ds_read_b128 v[150:153], v150
	ds_read_b128 v[154:157], v154
	ds_read_b128 v[158:161], v158
	s_mov_b32 m0, s47
	v_lshl_add_u64 v[240:241], s[36:37], 0, v[200:201]
	ds_read_b128 v[162:165], v221 offset:32768
	ds_read_b128 v[170:173], v221 offset:33792
	ds_read_b128 v[166:169], v223 offset:32768
	ds_read_b128 v[174:177], v223 offset:33792
	ds_read_b128 v[178:181], v221 offset:36864
	ds_read_b128 v[186:189], v221 offset:37888
	ds_read_b128 v[182:185], v223 offset:36864
	ds_read_b128 v[190:193], v223 offset:37888
	global_load_lds_dwordx4 v[240:241], off
	v_lshl_add_u64 v[240:241], s[36:37], 0, v[204:205]
	s_mov_b32 m0, s48
	s_nop 0
	global_load_lds_dwordx4 v[240:241], off
	s_waitcnt vmcnt(8)
	s_waitcnt lgkmcnt(0)
	s_barrier
	s_setprio 1
	s_waitcnt lgkmcnt(0)
	v_mfma_scale_f32_32x32x64_f8f6f4 v[114:129], v[130:137], v[162:169], v[114:129], v224, v224 op_sel_hi:[0,0,0]
	v_mfma_scale_f32_32x32x64_f8f6f4 v[82:97], v[130:137], v[178:185], v[82:97], v224, v224 op_sel_hi:[0,0,0]
	v_mfma_scale_f32_32x32x64_f8f6f4 v[114:129], v[138:145], v[170:177], v[114:129], v224, v224 op_sel_hi:[0,0,0]
	v_mfma_scale_f32_32x32x64_f8f6f4 v[82:97], v[138:145], v[186:193], v[82:97], v224, v224 op_sel_hi:[0,0,0]
	v_mfma_scale_f32_32x32x64_f8f6f4 v[98:113], v[146:153], v[162:169], v[98:113], v224, v224 op_sel_hi:[0,0,0]
	v_mfma_scale_f32_32x32x64_f8f6f4 v[66:81], v[146:153], v[178:185], v[66:81], v224, v224 op_sel_hi:[0,0,0]
	v_mfma_scale_f32_32x32x64_f8f6f4 v[98:113], v[154:161], v[170:177], v[98:113], v224, v224 op_sel_hi:[0,0,0]
	v_mfma_scale_f32_32x32x64_f8f6f4 v[66:81], v[154:161], v[186:193], v[66:81], v224, v224 op_sel_hi:[0,0,0]
	s_setprio 0
	s_barrier
	s_add_i32 s36, s65, s40
	v_lshl_add_u64 v[232:233], v[232:233], 0, s[14:15]
	s_mov_b32 m0, s36
	ds_read_b128 v[162:165], v221 offset:49152
	ds_read_b128 v[170:173], v221 offset:50176
	ds_read_b128 v[166:169], v223 offset:49152
	ds_read_b128 v[174:177], v223 offset:50176
	ds_read_b128 v[178:181], v221 offset:53248
	ds_read_b128 v[186:189], v221 offset:54272
	ds_read_b128 v[182:185], v223 offset:53248
	ds_read_b128 v[190:193], v223 offset:54272
	global_load_lds_dwordx4 v[232:233], off
	s_add_i32 m0, s36, 0x2000
	s_add_u32 s34, s34, 0x40080
	v_lshl_add_u64 v[232:233], v[234:235], 0, s[14:15]
	s_addc_u32 s35, s35, 0
	s_add_i32 s36, s66, s40
	global_load_lds_dwordx4 v[232:233], off
	v_lshl_add_u64 v[232:233], s[34:35], 0, v[194:195]
	s_mov_b32 m0, s36
	s_nop 0
	global_load_lds_dwordx4 v[232:233], off
	v_lshl_add_u64 v[232:233], s[34:35], 0, v[196:197]
	s_add_i32 m0, s36, 0x2000
	s_nop 0
	global_load_lds_dwordx4 v[232:233], off
	s_waitcnt vmcnt(6)
	s_waitcnt lgkmcnt(0)
	s_barrier
	s_setprio 1
	s_waitcnt lgkmcnt(0)
	v_mfma_scale_f32_32x32x64_f8f6f4 v[50:65], v[130:137], v[162:169], v[50:65], v224, v224 op_sel_hi:[0,0,0]
	v_mfma_scale_f32_32x32x64_f8f6f4 v[18:33], v[130:137], v[178:185], v[18:33], v224, v224 op_sel_hi:[0,0,0]
	v_mfma_scale_f32_32x32x64_f8f6f4 v[50:65], v[138:145], v[170:177], v[50:65], v224, v224 op_sel_hi:[0,0,0]
	v_lshl_add_u64 v[232:233], v[236:237], 0, s[14:15]
	s_mov_b32 m0, s52
	s_nop 0
	global_load_lds_dwordx4 v[232:233], off
	v_mfma_scale_f32_32x32x64_f8f6f4 v[18:33], v[138:145], v[186:193], v[18:33], v224, v224 op_sel_hi:[0,0,0]
	v_mfma_scale_f32_32x32x64_f8f6f4 v[34:49], v[146:153], v[162:169], v[34:49], v224, v224 op_sel_hi:[0,0,0]
	v_mfma_scale_f32_32x32x64_f8f6f4 v[2:17], v[146:153], v[178:185], v[2:17], v224, v224 op_sel_hi:[0,0,0]
	v_lshl_add_u64 v[232:233], v[238:239], 0, s[14:15]
	s_mov_b32 m0, s53
	s_nop 0
	global_load_lds_dwordx4 v[232:233], off
	v_mfma_scale_f32_32x32x64_f8f6f4 v[34:49], v[154:161], v[170:177], v[34:49], v224, v224 op_sel_hi:[0,0,0]
	v_mfma_scale_f32_32x32x64_f8f6f4 v[2:17], v[154:161], v[186:193], v[2:17], v224, v224 op_sel_hi:[0,0,0]
	s_setprio 0
	s_barrier
	s_add_i32 s64, s64, 2
	s_add_u32 s30, s30, 0x100
	s_addc_u32 s31, s31, 0
	s_add_u32 s25, s25, 0x100
	s_addc_u32 s27, s27, 0
	s_cmp_gt_u32 s64, 13
	s_cbranch_scc1 .LBB0_928

.LBB0_1014:
	ds_read_b128 v[168:171], v150
	ds_read_b128 v[172:175], v151
	ds_read_b128 v[176:179], v152
	ds_read_b128 v[180:183], v153
	ds_read_b128 v[184:187], v154
	ds_read_b128 v[188:191], v155
	ds_read_b128 v[192:195], v156
	ds_read_b128 v[196:199], v157
	s_add_u32 s30, s28, 0xfffe0080
	s_addc_u32 s31, s29, -1
	s_cmp_eq_u32 s58, 4
	s_cselect_b32 s35, s21, s31
	s_cselect_b32 s34, s20, s30
	s_cselect_b32 s31, s23, s27
	s_cselect_b32 s30, s22, s25
	v_lshl_add_u64 v[144:145], s[28:29], 0, v[140:141]
	s_add_i32 m0, s37, 0xc000
	ds_read_b128 v[200:203], v158
	ds_read_b128 v[208:211], v158 offset:1024
	ds_read_b128 v[204:207], v159
	ds_read_b128 v[212:215], v159 offset:1024
	ds_read_b128 v[216:219], v158 offset:4096
	ds_read_b128 v[224:227], v158 offset:5120
	ds_read_b128 v[220:223], v159 offset:4096
	ds_read_b128 v[228:231], v159 offset:5120
	global_load_lds_dwordx4 v[144:145], off
	v_lshl_add_u64 v[144:145], s[28:29], 0, v[142:143]
	s_add_i32 m0, s37, 0xe000
	s_nop 0
	global_load_lds_dwordx4 v[144:145], off
	s_waitcnt vmcnt(8)
	s_waitcnt lgkmcnt(0)
	s_barrier
	s_setprio 1
	s_waitcnt lgkmcnt(0)
	v_mfma_scale_f32_32x32x64_f8f6f4 v[114:129], v[168:175], v[200:207], v[114:129], v160, v160 op_sel_hi:[0,0,0]
	v_mfma_scale_f32_32x32x64_f8f6f4 v[82:97], v[168:175], v[216:223], v[82:97], v160, v160 op_sel_hi:[0,0,0]
	v_mfma_scale_f32_32x32x64_f8f6f4 v[114:129], v[176:183], v[208:215], v[114:129], v160, v160 op_sel_hi:[0,0,0]
	v_mfma_scale_f32_32x32x64_f8f6f4 v[82:97], v[176:183], v[224:231], v[82:97], v160, v160 op_sel_hi:[0,0,0]
	v_mfma_scale_f32_32x32x64_f8f6f4 v[98:113], v[184:191], v[200:207], v[98:113], v160, v160 op_sel_hi:[0,0,0]
	v_mfma_scale_f32_32x32x64_f8f6f4 v[66:81], v[184:191], v[216:223], v[66:81], v160, v160 op_sel_hi:[0,0,0]
	v_mfma_scale_f32_32x32x64_f8f6f4 v[98:113], v[192:199], v[208:215], v[98:113], v160, v160 op_sel_hi:[0,0,0]
	v_mfma_scale_f32_32x32x64_f8f6f4 v[66:81], v[192:199], v[224:231], v[66:81], v160, v160 op_sel_hi:[0,0,0]
	s_setprio 0
	s_barrier
	s_add_i32 s59, s51, s36
	v_lshl_add_u64 v[144:145], s[30:31], 0, v[132:133]
	s_mov_b32 m0, s59
	ds_read_b128 v[200:203], v158 offset:16384
	ds_read_b128 v[208:211], v158 offset:17408
	ds_read_b128 v[204:207], v159 offset:16384
	ds_read_b128 v[212:215], v159 offset:17408
	ds_read_b128 v[216:219], v158 offset:20480
	ds_read_b128 v[224:227], v158 offset:21504
	ds_read_b128 v[220:223], v159 offset:20480
	ds_read_b128 v[228:231], v159 offset:21504
	global_load_lds_dwordx4 v[144:145], off
	s_add_i32 m0, s59, 0x2000
	s_add_u32 s60, s30, 0x20000
	v_lshl_add_u64 v[146:147], s[30:31], 0, v[136:137]
	s_addc_u32 s61, s31, 0
	s_add_i32 s59, s52, s36
	global_load_lds_dwordx4 v[146:147], off
	v_lshl_add_u64 v[232:233], s[60:61], 0, v[132:133]
	s_mov_b32 m0, s59
	v_lshl_add_u64 v[234:235], s[34:35], 0, v[134:135]
	global_load_lds_dwordx4 v[232:233], off
	v_lshl_add_u64 v[232:233], s[60:61], 0, v[136:137]
	s_add_i32 m0, s59, 0x2000
	s_nop 0
	global_load_lds_dwordx4 v[232:233], off
	s_waitcnt vmcnt(6)
	s_waitcnt lgkmcnt(0)
	s_barrier
	s_setprio 1
	s_waitcnt lgkmcnt(0)
	v_mfma_scale_f32_32x32x64_f8f6f4 v[50:65], v[168:175], v[200:207], v[50:65], v160, v160 op_sel_hi:[0,0,0]
	v_mfma_scale_f32_32x32x64_f8f6f4 v[18:33], v[168:175], v[216:223], v[18:33], v160, v160 op_sel_hi:[0,0,0]
	v_mfma_scale_f32_32x32x64_f8f6f4 v[50:65], v[176:183], v[208:215], v[50:65], v160, v160 op_sel_hi:[0,0,0]
	v_lshl_add_u64 v[232:233], s[34:35], 0, v[130:131]
	s_mov_b32 m0, s37
	s_nop 0
	global_load_lds_dwordx4 v[232:233], off
	v_mfma_scale_f32_32x32x64_f8f6f4 v[18:33], v[176:183], v[224:231], v[18:33], v160, v160 op_sel_hi:[0,0,0]
	v_mfma_scale_f32_32x32x64_f8f6f4 v[34:49], v[184:191], v[200:207], v[34:49], v160, v160 op_sel_hi:[0,0,0]
	v_mfma_scale_f32_32x32x64_f8f6f4 v[2:17], v[184:191], v[216:223], v[2:17], v160, v160 op_sel_hi:[0,0,0]
	s_mov_b32 m0, s38
	s_nop 0
	global_load_lds_dwordx4 v[234:235], off
	v_mfma_scale_f32_32x32x64_f8f6f4 v[34:49], v[192:199], v[208:215], v[34:49], v160, v160 op_sel_hi:[0,0,0]
	v_mfma_scale_f32_32x32x64_f8f6f4 v[2:17], v[192:199], v[224:231], v[2:17], v160, v160 op_sel_hi:[0,0,0]
	s_setprio 0
	s_barrier
	s_add_i32 s59, 0, 0x18000
	v_add_u32_e32 v167, s59, v1
	v_add_u32_e32 v172, s59, v148
	s_add_i32 s60, 0, 0x1c000
	ds_read_b128 v[168:171], v167
	ds_read_b128 v[172:175], v172
	ds_read_b128 v[176:179], v161
	ds_read_b128 v[180:183], v162
	v_add_u32_e32 v167, s60, v1
	v_add_u32_e32 v188, s60, v148
	ds_read_b128 v[184:187], v167
	ds_read_b128 v[188:191], v188
	ds_read_b128 v[192:195], v163
	ds_read_b128 v[196:199], v164
	s_add_u32 s34, s34, 0x20000
	s_addc_u32 s35, s35, 0
	s_mov_b32 m0, s39
	v_lshl_add_u64 v[236:237], s[34:35], 0, v[130:131]
	ds_read_b128 v[200:203], v158 offset:32768
	ds_read_b128 v[208:211], v158 offset:33792
	ds_read_b128 v[204:207], v159 offset:32768
	ds_read_b128 v[212:215], v159 offset:33792
	ds_read_b128 v[216:219], v158 offset:36864
	ds_read_b128 v[224:227], v158 offset:37888
	ds_read_b128 v[220:223], v159 offset:36864
	ds_read_b128 v[228:231], v159 offset:37888
	global_load_lds_dwordx4 v[236:237], off
	v_lshl_add_u64 v[236:237], s[34:35], 0, v[134:135]
	s_mov_b32 m0, s40
	s_nop 0
	global_load_lds_dwordx4 v[236:237], off
	s_waitcnt vmcnt(8)
	s_waitcnt lgkmcnt(0)
	s_barrier
	s_setprio 1
	s_waitcnt lgkmcnt(0)
	v_mfma_scale_f32_32x32x64_f8f6f4 v[114:129], v[168:175], v[200:207], v[114:129], v160, v160 op_sel_hi:[0,0,0]
	v_mfma_scale_f32_32x32x64_f8f6f4 v[82:97], v[168:175], v[216:223], v[82:97], v160, v160 op_sel_hi:[0,0,0]
	v_mfma_scale_f32_32x32x64_f8f6f4 v[114:129], v[176:183], v[208:215], v[114:129], v160, v160 op_sel_hi:[0,0,0]
	v_mfma_scale_f32_32x32x64_f8f6f4 v[82:97], v[176:183], v[224:231], v[82:97], v160, v160 op_sel_hi:[0,0,0]
	v_mfma_scale_f32_32x32x64_f8f6f4 v[98:113], v[184:191], v[200:207], v[98:113], v160, v160 op_sel_hi:[0,0,0]
	v_mfma_scale_f32_32x32x64_f8f6f4 v[66:81], v[184:191], v[216:223], v[66:81], v160, v160 op_sel_hi:[0,0,0]
	v_mfma_scale_f32_32x32x64_f8f6f4 v[98:113], v[192:199], v[208:215], v[98:113], v160, v160 op_sel_hi:[0,0,0]
	v_mfma_scale_f32_32x32x64_f8f6f4 v[66:81], v[192:199], v[224:231], v[66:81], v160, v160 op_sel_hi:[0,0,0]
	s_setprio 0
	s_barrier
	s_add_i32 s34, s59, s36
	v_lshl_add_u64 v[144:145], v[144:145], 0, s[12:13]
	s_mov_b32 m0, s34
	ds_read_b128 v[200:203], v158 offset:49152
	ds_read_b128 v[208:211], v158 offset:50176
	ds_read_b128 v[204:207], v159 offset:49152
	ds_read_b128 v[212:215], v159 offset:50176
	ds_read_b128 v[216:219], v158 offset:53248
	ds_read_b128 v[224:227], v158 offset:54272
	ds_read_b128 v[220:223], v159 offset:53248
	ds_read_b128 v[228:231], v159 offset:54272
	global_load_lds_dwordx4 v[144:145], off
	s_add_i32 m0, s34, 0x2000
	s_add_u32 s30, s30, 0x20080
	v_lshl_add_u64 v[144:145], v[146:147], 0, s[12:13]
	s_addc_u32 s31, s31, 0
	s_add_i32 s34, s60, s36
	global_load_lds_dwordx4 v[144:145], off
	v_lshl_add_u64 v[144:145], s[30:31], 0, v[132:133]
	s_mov_b32 m0, s34
	s_nop 0
	global_load_lds_dwordx4 v[144:145], off
	v_lshl_add_u64 v[144:145], s[30:31], 0, v[136:137]
	s_add_i32 m0, s34, 0x2000
	s_nop 0
	global_load_lds_dwordx4 v[144:145], off
	s_waitcnt vmcnt(6)
	s_waitcnt lgkmcnt(0)
	s_barrier
	s_setprio 1
	s_waitcnt lgkmcnt(0)
	v_mfma_scale_f32_32x32x64_f8f6f4 v[50:65], v[168:175], v[200:207], v[50:65], v160, v160 op_sel_hi:[0,0,0]
	v_mfma_scale_f32_32x32x64_f8f6f4 v[18:33], v[168:175], v[216:223], v[18:33], v160, v160 op_sel_hi:[0,0,0]
	v_mfma_scale_f32_32x32x64_f8f6f4 v[50:65], v[176:183], v[208:215], v[50:65], v160, v160 op_sel_hi:[0,0,0]
	v_lshl_add_u64 v[144:145], v[232:233], 0, s[12:13]
	s_mov_b32 m0, s46
	s_nop 0
	global_load_lds_dwordx4 v[144:145], off
	v_mfma_scale_f32_32x32x64_f8f6f4 v[18:33], v[176:183], v[224:231], v[18:33], v160, v160 op_sel_hi:[0,0,0]
	v_mfma_scale_f32_32x32x64_f8f6f4 v[34:49], v[184:191], v[200:207], v[34:49], v160, v160 op_sel_hi:[0,0,0]
	v_mfma_scale_f32_32x32x64_f8f6f4 v[2:17], v[184:191], v[216:223], v[2:17], v160, v160 op_sel_hi:[0,0,0]
	v_lshl_add_u64 v[144:145], v[234:235], 0, s[12:13]
	s_mov_b32 m0, s47
	s_nop 0
	global_load_lds_dwordx4 v[144:145], off
	v_mfma_scale_f32_32x32x64_f8f6f4 v[34:49], v[192:199], v[208:215], v[34:49], v160, v160 op_sel_hi:[0,0,0]
	v_mfma_scale_f32_32x32x64_f8f6f4 v[2:17], v[192:199], v[224:231], v[2:17], v160, v160 op_sel_hi:[0,0,0]
	s_setprio 0
	s_barrier
	s_add_i32 s58, s58, 2
	s_add_u32 s28, s28, 0x100
	s_addc_u32 s29, s29, 0
	s_add_u32 s25, s25, 0x100
	s_addc_u32 s27, s27, 0
	s_cmp_gt_u32 s58, 5
	s_cbranch_scc0 .LBB0_1014
	s_and_b64 vcc, exec, s[14:15]
	s_cbranch_vccz .LBB0_1017
	s_barrier

.LBB0_1147:
	v_add_u32_e32 v130, s63, v1
	v_add_u32_e32 v134, s63, v177
	v_add_u32_e32 v146, s64, v1
	v_add_u32_e32 v150, s64, v177
	ds_read_b128 v[130:133], v130
	ds_read_b128 v[134:137], v134
	ds_read_b128 v[138:141], v179
	ds_read_b128 v[142:145], v181
	ds_read_b128 v[146:149], v146
	ds_read_b128 v[150:153], v150
	ds_read_b128 v[154:157], v183
	ds_read_b128 v[158:161], v190
	s_add_u32 s42, s40, 0xfffc0080
	s_addc_u32 s43, s41, -1
	s_cmp_eq_u32 s35, 12
	s_cselect_b32 s45, s37, s43
	s_cselect_b32 s44, s36, s42
	s_cselect_b32 s43, s39, s31
	s_cselect_b32 s42, s38, s7
	v_lshl_add_u64 v[184:185], s[40:41], 0, v[172:173]
	s_add_i32 m0, s51, 0xc000
	ds_read_b128 v[208:211], v191
	ds_read_b128 v[216:219], v191 offset:1024
	ds_read_b128 v[212:215], v192
	ds_read_b128 v[220:223], v192 offset:1024
	ds_read_b128 v[224:227], v191 offset:4096
	ds_read_b128 v[232:235], v191 offset:5120
	ds_read_b128 v[228:231], v192 offset:4096
	ds_read_b128 v[236:239], v192 offset:5120
	global_load_lds_dwordx4 v[184:185], off
	v_lshl_add_u64 v[184:185], s[40:41], 0, v[174:175]
	s_add_i32 m0, s51, 0xe000
	s_nop 0
	global_load_lds_dwordx4 v[184:185], off
	s_waitcnt vmcnt(8)
	s_waitcnt lgkmcnt(0)
	s_barrier
	s_setprio 1
	s_waitcnt lgkmcnt(0)
	v_mfma_scale_f32_32x32x64_f8f6f4 v[114:129], v[130:137], v[208:215], v[114:129], v193, v193 op_sel_hi:[0,0,0]
	v_mfma_scale_f32_32x32x64_f8f6f4 v[82:97], v[130:137], v[224:231], v[82:97], v193, v193 op_sel_hi:[0,0,0]
	v_mfma_scale_f32_32x32x64_f8f6f4 v[114:129], v[138:145], v[216:223], v[114:129], v193, v193 op_sel_hi:[0,0,0]
	v_mfma_scale_f32_32x32x64_f8f6f4 v[82:97], v[138:145], v[232:239], v[82:97], v193, v193 op_sel_hi:[0,0,0]
	v_mfma_scale_f32_32x32x64_f8f6f4 v[98:113], v[146:153], v[208:215], v[98:113], v193, v193 op_sel_hi:[0,0,0]
	v_mfma_scale_f32_32x32x64_f8f6f4 v[66:81], v[146:153], v[224:231], v[66:81], v193, v193 op_sel_hi:[0,0,0]
	v_mfma_scale_f32_32x32x64_f8f6f4 v[98:113], v[154:161], v[216:223], v[98:113], v193, v193 op_sel_hi:[0,0,0]
	v_mfma_scale_f32_32x32x64_f8f6f4 v[66:81], v[154:161], v[232:239], v[66:81], v193, v193 op_sel_hi:[0,0,0]
	s_setprio 0
	s_barrier
	s_add_i32 s46, s63, s50
	v_lshl_add_u64 v[184:185], s[42:43], 0, v[164:165]
	s_mov_b32 m0, s46
	ds_read_b128 v[208:211], v191 offset:16384
	ds_read_b128 v[216:219], v191 offset:17408
	ds_read_b128 v[212:215], v192 offset:16384
	ds_read_b128 v[220:223], v192 offset:17408
	ds_read_b128 v[224:227], v191 offset:20480
	ds_read_b128 v[232:235], v191 offset:21504
	ds_read_b128 v[228:231], v192 offset:20480
	ds_read_b128 v[236:239], v192 offset:21504
	global_load_lds_dwordx4 v[184:185], off
	s_add_i32 m0, s46, 0x2000
	s_add_u32 s46, s42, 0x40000
	v_lshl_add_u64 v[186:187], s[42:43], 0, v[168:169]
	s_addc_u32 s47, s43, 0
	s_add_i32 s70, s64, s50
	global_load_lds_dwordx4 v[186:187], off
	v_lshl_add_u64 v[188:189], s[46:47], 0, v[164:165]
	s_mov_b32 m0, s70
	v_lshl_add_u64 v[240:241], s[44:45], 0, v[166:167]
	global_load_lds_dwordx4 v[188:189], off
	v_lshl_add_u64 v[188:189], s[46:47], 0, v[168:169]
	s_add_i32 m0, s70, 0x2000
	s_nop 0
	global_load_lds_dwordx4 v[188:189], off
	s_waitcnt vmcnt(6)
	s_waitcnt lgkmcnt(0)
	s_barrier
	s_setprio 1
	s_waitcnt lgkmcnt(0)
	v_mfma_scale_f32_32x32x64_f8f6f4 v[50:65], v[130:137], v[208:215], v[50:65], v193, v193 op_sel_hi:[0,0,0]
	v_mfma_scale_f32_32x32x64_f8f6f4 v[18:33], v[130:137], v[224:231], v[18:33], v193, v193 op_sel_hi:[0,0,0]
	v_mfma_scale_f32_32x32x64_f8f6f4 v[50:65], v[138:145], v[216:223], v[50:65], v193, v193 op_sel_hi:[0,0,0]
	v_lshl_add_u64 v[188:189], s[44:45], 0, v[162:163]
	s_mov_b32 m0, s51
	s_nop 0
	global_load_lds_dwordx4 v[188:189], off
	v_mfma_scale_f32_32x32x64_f8f6f4 v[18:33], v[138:145], v[232:239], v[18:33], v193, v193 op_sel_hi:[0,0,0]
	v_mfma_scale_f32_32x32x64_f8f6f4 v[34:49], v[146:153], v[208:215], v[34:49], v193, v193 op_sel_hi:[0,0,0]
	v_mfma_scale_f32_32x32x64_f8f6f4 v[2:17], v[146:153], v[224:231], v[2:17], v193, v193 op_sel_hi:[0,0,0]
	s_mov_b32 m0, s52
	s_nop 0
	global_load_lds_dwordx4 v[240:241], off
	v_mfma_scale_f32_32x32x64_f8f6f4 v[34:49], v[154:161], v[216:223], v[34:49], v193, v193 op_sel_hi:[0,0,0]
	v_mfma_scale_f32_32x32x64_f8f6f4 v[2:17], v[154:161], v[232:239], v[2:17], v193, v193 op_sel_hi:[0,0,0]
	s_setprio 0
	s_barrier
	s_add_i32 s46, 0, 0x18000
	s_add_i32 s47, 0, 0x1c000
	v_add_u32_e32 v130, s46, v1
	v_add_u32_e32 v134, s46, v177
	v_add_u32_e32 v146, s47, v1
	v_add_u32_e32 v150, s47, v177
	ds_read_b128 v[130:133], v130
	ds_read_b128 v[134:137], v134
	ds_read_b128 v[138:141], v194
	ds_read_b128 v[142:145], v195
	ds_read_b128 v[146:149], v146
	ds_read_b128 v[150:153], v150
	ds_read_b128 v[154:157], v196
	ds_read_b128 v[158:161], v197
	s_add_u32 s44, s44, 0x40000
	s_addc_u32 s45, s45, 0
	s_mov_b32 m0, s53
	v_lshl_add_u64 v[242:243], s[44:45], 0, v[162:163]
	ds_read_b128 v[208:211], v191 offset:32768
	ds_read_b128 v[216:219], v191 offset:33792
	ds_read_b128 v[212:215], v192 offset:32768
	ds_read_b128 v[220:223], v192 offset:33792
	ds_read_b128 v[224:227], v191 offset:36864
	ds_read_b128 v[232:235], v191 offset:37888
	ds_read_b128 v[228:231], v192 offset:36864
	ds_read_b128 v[236:239], v192 offset:37888
	global_load_lds_dwordx4 v[242:243], off
	v_lshl_add_u64 v[242:243], s[44:45], 0, v[166:167]
	s_mov_b32 m0, s54
	s_nop 0
	global_load_lds_dwordx4 v[242:243], off
	s_waitcnt vmcnt(8)
	s_waitcnt lgkmcnt(0)
	s_barrier
	s_setprio 1
	s_waitcnt lgkmcnt(0)
	v_mfma_scale_f32_32x32x64_f8f6f4 v[114:129], v[130:137], v[208:215], v[114:129], v193, v193 op_sel_hi:[0,0,0]
	v_mfma_scale_f32_32x32x64_f8f6f4 v[82:97], v[130:137], v[224:231], v[82:97], v193, v193 op_sel_hi:[0,0,0]
	v_mfma_scale_f32_32x32x64_f8f6f4 v[114:129], v[138:145], v[216:223], v[114:129], v193, v193 op_sel_hi:[0,0,0]
	v_mfma_scale_f32_32x32x64_f8f6f4 v[82:97], v[138:145], v[232:239], v[82:97], v193, v193 op_sel_hi:[0,0,0]
	v_mfma_scale_f32_32x32x64_f8f6f4 v[98:113], v[146:153], v[208:215], v[98:113], v193, v193 op_sel_hi:[0,0,0]
	v_mfma_scale_f32_32x32x64_f8f6f4 v[66:81], v[146:153], v[224:231], v[66:81], v193, v193 op_sel_hi:[0,0,0]
	v_mfma_scale_f32_32x32x64_f8f6f4 v[98:113], v[154:161], v[216:223], v[98:113], v193, v193 op_sel_hi:[0,0,0]
	v_mfma_scale_f32_32x32x64_f8f6f4 v[66:81], v[154:161], v[232:239], v[66:81], v193, v193 op_sel_hi:[0,0,0]
	s_setprio 0
	s_barrier
	s_add_i32 s44, s46, s50
	v_lshl_add_u64 v[184:185], v[184:185], 0, s[20:21]
	s_mov_b32 m0, s44
	ds_read_b128 v[208:211], v191 offset:49152
	ds_read_b128 v[216:219], v191 offset:50176
	ds_read_b128 v[212:215], v192 offset:49152
	ds_read_b128 v[220:223], v192 offset:50176
	ds_read_b128 v[224:227], v191 offset:53248
	ds_read_b128 v[232:235], v191 offset:54272
	ds_read_b128 v[228:231], v192 offset:53248
	ds_read_b128 v[236:239], v192 offset:54272
	global_load_lds_dwordx4 v[184:185], off
	s_add_i32 m0, s44, 0x2000
	s_add_u32 s42, s42, 0x40080
	v_lshl_add_u64 v[184:185], v[186:187], 0, s[20:21]
	s_addc_u32 s43, s43, 0
	s_add_i32 s44, s47, s50
	global_load_lds_dwordx4 v[184:185], off
	v_lshl_add_u64 v[184:185], s[42:43], 0, v[164:165]
	s_mov_b32 m0, s44
	s_nop 0
	global_load_lds_dwordx4 v[184:185], off
	v_lshl_add_u64 v[184:185], s[42:43], 0, v[168:169]
	s_add_i32 m0, s44, 0x2000
	s_nop 0
	global_load_lds_dwordx4 v[184:185], off
	s_waitcnt vmcnt(6)
	s_waitcnt lgkmcnt(0)
	s_barrier
	s_setprio 1
	s_waitcnt lgkmcnt(0)
	v_mfma_scale_f32_32x32x64_f8f6f4 v[50:65], v[130:137], v[208:215], v[50:65], v193, v193 op_sel_hi:[0,0,0]
	v_mfma_scale_f32_32x32x64_f8f6f4 v[18:33], v[130:137], v[224:231], v[18:33], v193, v193 op_sel_hi:[0,0,0]
	v_mfma_scale_f32_32x32x64_f8f6f4 v[50:65], v[138:145], v[216:223], v[50:65], v193, v193 op_sel_hi:[0,0,0]
	v_lshl_add_u64 v[184:185], v[188:189], 0, s[20:21]
	s_mov_b32 m0, s57
	s_nop 0
	global_load_lds_dwordx4 v[184:185], off
	v_mfma_scale_f32_32x32x64_f8f6f4 v[18:33], v[138:145], v[232:239], v[18:33], v193, v193 op_sel_hi:[0,0,0]
	v_mfma_scale_f32_32x32x64_f8f6f4 v[34:49], v[146:153], v[208:215], v[34:49], v193, v193 op_sel_hi:[0,0,0]
	v_mfma_scale_f32_32x32x64_f8f6f4 v[2:17], v[146:153], v[224:231], v[2:17], v193, v193 op_sel_hi:[0,0,0]
	v_lshl_add_u64 v[184:185], v[240:241], 0, s[20:21]
	s_mov_b32 m0, s58
	s_nop 0
	global_load_lds_dwordx4 v[184:185], off
	v_mfma_scale_f32_32x32x64_f8f6f4 v[34:49], v[154:161], v[216:223], v[34:49], v193, v193 op_sel_hi:[0,0,0]
	v_mfma_scale_f32_32x32x64_f8f6f4 v[2:17], v[154:161], v[232:239], v[2:17], v193, v193 op_sel_hi:[0,0,0]
	s_setprio 0
	s_barrier
	s_add_i32 s35, s35, 2
	s_add_u32 s40, s40, 0x100
	s_addc_u32 s41, s41, 0
	s_add_u32 s7, s7, 0x100
	s_addc_u32 s31, s31, 0
	s_cmp_gt_u32 s35, 13
	s_cbranch_scc0 .LBB0_1147
	s_and_b64 vcc, exec, s[22:23]
	s_cbranch_vccz .LBB0_1150
	s_barrier

.LBB0_1536:
	s_waitcnt vmcnt(8)
	s_add_u32 s34, s28, 0x80
	s_waitcnt lgkmcnt(0)
	s_addc_u32 s35, s29, 0
	s_and_b64 s[30:31], s[30:31], exec
	v_mov_b32_e32 v205, v199
	s_cselect_b32 s35, s9, s35
	s_cselect_b32 s34, s8, s34
	s_cselect_b32 s31, s21, s25
	s_cselect_b32 s30, s20, s23
	s_barrier
	s_setprio 1
	s_waitcnt lgkmcnt(0)
	v_mfma_scale_f32_32x32x64_f8f6f4 v[114:129], v[154:161], v[178:185], v[114:129], v224, v224 op_sel_hi:[0,0,0]
	v_mfma_scale_f32_32x32x64_f8f6f4 v[82:97], v[154:161], v[186:193], v[82:97], v224, v224 op_sel_hi:[0,0,0]
	v_mfma_scale_f32_32x32x64_f8f6f4 v[114:129], v[146:153], v[162:169], v[114:129], v224, v224 op_sel_hi:[0,0,0]
	v_mfma_scale_f32_32x32x64_f8f6f4 v[82:97], v[146:153], v[170:177], v[82:97], v224, v224 op_sel_hi:[0,0,0]
	v_mfma_scale_f32_32x32x64_f8f6f4 v[98:113], v[138:145], v[178:185], v[98:113], v224, v224 op_sel_hi:[0,0,0]
	v_mfma_scale_f32_32x32x64_f8f6f4 v[66:81], v[138:145], v[186:193], v[66:81], v224, v224 op_sel_hi:[0,0,0]
	v_mfma_scale_f32_32x32x64_f8f6f4 v[98:113], v[130:137], v[162:169], v[98:113], v224, v224 op_sel_hi:[0,0,0]
	v_mfma_scale_f32_32x32x64_f8f6f4 v[66:81], v[130:137], v[170:177], v[66:81], v224, v224 op_sel_hi:[0,0,0]
	s_setprio 0
	s_barrier
	s_mov_b32 m0, s40
	v_lshl_add_u64 v[232:233], s[30:31], 0, v[194:195]
	s_add_u32 s64, s30, 0x40000
	ds_read_b128 v[162:165], v221 offset:16384
	ds_read_b128 v[170:173], v221 offset:17408
	ds_read_b128 v[166:169], v223 offset:16384
	ds_read_b128 v[174:177], v223 offset:17408
	ds_read_b128 v[178:181], v221 offset:20480
	ds_read_b128 v[186:189], v221 offset:21504
	ds_read_b128 v[182:185], v223 offset:20480
	ds_read_b128 v[190:193], v223 offset:21504
	global_load_lds_dwordx4 v[232:233], off
	v_lshl_add_u64 v[234:235], s[30:31], 0, v[196:197]
	s_mov_b32 m0, s41
	s_addc_u32 s65, s31, 0
	global_load_lds_dwordx4 v[234:235], off
	v_lshl_add_u64 v[236:237], s[64:65], 0, v[194:195]
	s_mov_b32 m0, s42
	v_mov_b32_e32 v203, v199
	global_load_lds_dwordx4 v[236:237], off
	v_lshl_add_u64 v[236:237], s[64:65], 0, v[196:197]
	s_mov_b32 m0, s43
	v_lshl_add_u64 v[238:239], s[34:35], 0, v[202:203]
	global_load_lds_dwordx4 v[236:237], off
	s_waitcnt vmcnt(6)
	s_waitcnt lgkmcnt(0)
	s_barrier
	s_setprio 1
	s_waitcnt lgkmcnt(0)
	v_mfma_scale_f32_32x32x64_f8f6f4 v[50:65], v[154:161], v[162:169], v[50:65], v224, v224 op_sel_hi:[0,0,0]
	v_mfma_scale_f32_32x32x64_f8f6f4 v[18:33], v[154:161], v[178:185], v[18:33], v224, v224 op_sel_hi:[0,0,0]
	v_mfma_scale_f32_32x32x64_f8f6f4 v[50:65], v[146:153], v[170:177], v[50:65], v224, v224 op_sel_hi:[0,0,0]
	s_mov_b32 m0, s39
	v_lshl_add_u64 v[236:237], s[34:35], 0, v[198:199]
	global_load_lds_dwordx4 v198, s[34:35]
	v_mfma_scale_f32_32x32x64_f8f6f4 v[18:33], v[146:153], v[186:193], v[18:33], v224, v224 op_sel_hi:[0,0,0]
	v_mfma_scale_f32_32x32x64_f8f6f4 v[34:49], v[138:145], v[162:169], v[34:49], v224, v224 op_sel_hi:[0,0,0]
	v_mfma_scale_f32_32x32x64_f8f6f4 v[2:17], v[138:145], v[178:185], v[2:17], v224, v224 op_sel_hi:[0,0,0]
	s_mov_b32 m0, s44
	s_nop 0
	global_load_lds_dwordx4 v202, s[34:35]
	v_mfma_scale_f32_32x32x64_f8f6f4 v[34:49], v[130:137], v[170:177], v[34:49], v224, v224 op_sel_hi:[0,0,0]
	v_mfma_scale_f32_32x32x64_f8f6f4 v[2:17], v[130:137], v[186:193], v[2:17], v224, v224 op_sel_hi:[0,0,0]
	s_setprio 0
	s_barrier
	s_add_i32 s63, 0, 0x18000
	s_add_i32 s64, 0, 0x1c000
	v_add_u32_e32 v130, s63, v210
	v_add_u32_e32 v134, s63, v211
	v_add_u32_e32 v138, s55, v210
	v_add_u32_e32 v142, s55, v211
	v_add_u32_e32 v146, s64, v210
	v_add_u32_e32 v150, s64, v211
	v_add_u32_e32 v154, s56, v210
	v_add_u32_e32 v158, s56, v211
	ds_read_b128 v[130:133], v130
	ds_read_b128 v[134:137], v134
	ds_read_b128 v[138:141], v138
	ds_read_b128 v[142:145], v142
	ds_read_b128 v[146:149], v146
	ds_read_b128 v[150:153], v150
	ds_read_b128 v[154:157], v154
	ds_read_b128 v[158:161], v158
	s_mov_b32 m0, s45
	v_lshl_add_u64 v[240:241], s[34:35], 0, v[200:201]
	ds_read_b128 v[162:165], v221 offset:32768
	ds_read_b128 v[170:173], v221 offset:33792
	ds_read_b128 v[166:169], v223 offset:32768
	ds_read_b128 v[174:177], v223 offset:33792
	ds_read_b128 v[178:181], v221 offset:36864
	ds_read_b128 v[186:189], v221 offset:37888
	ds_read_b128 v[182:185], v223 offset:36864
	ds_read_b128 v[190:193], v223 offset:37888
	global_load_lds_dwordx4 v[240:241], off
	v_lshl_add_u64 v[240:241], s[34:35], 0, v[204:205]
	s_mov_b32 m0, s46
	s_nop 0
	global_load_lds_dwordx4 v[240:241], off
	s_waitcnt vmcnt(8)
	s_waitcnt lgkmcnt(0)
	s_barrier
	s_setprio 1
	s_waitcnt lgkmcnt(0)
	v_mfma_scale_f32_32x32x64_f8f6f4 v[114:129], v[130:137], v[162:169], v[114:129], v224, v224 op_sel_hi:[0,0,0]
	v_mfma_scale_f32_32x32x64_f8f6f4 v[82:97], v[130:137], v[178:185], v[82:97], v224, v224 op_sel_hi:[0,0,0]
	v_mfma_scale_f32_32x32x64_f8f6f4 v[114:129], v[138:145], v[170:177], v[114:129], v224, v224 op_sel_hi:[0,0,0]
	v_mfma_scale_f32_32x32x64_f8f6f4 v[82:97], v[138:145], v[186:193], v[82:97], v224, v224 op_sel_hi:[0,0,0]
	v_mfma_scale_f32_32x32x64_f8f6f4 v[98:113], v[146:153], v[162:169], v[98:113], v224, v224 op_sel_hi:[0,0,0]
	v_mfma_scale_f32_32x32x64_f8f6f4 v[66:81], v[146:153], v[178:185], v[66:81], v224, v224 op_sel_hi:[0,0,0]
	v_mfma_scale_f32_32x32x64_f8f6f4 v[98:113], v[154:161], v[170:177], v[98:113], v224, v224 op_sel_hi:[0,0,0]
	v_mfma_scale_f32_32x32x64_f8f6f4 v[66:81], v[154:161], v[186:193], v[66:81], v224, v224 op_sel_hi:[0,0,0]
	s_setprio 0
	s_barrier
	s_add_i32 s34, s63, s38
	v_lshl_add_u64 v[232:233], v[232:233], 0, s[12:13]
	s_mov_b32 m0, s34
	ds_read_b128 v[162:165], v221 offset:49152
	ds_read_b128 v[170:173], v221 offset:50176
	ds_read_b128 v[166:169], v223 offset:49152
	ds_read_b128 v[174:177], v223 offset:50176
	ds_read_b128 v[178:181], v221 offset:53248
	ds_read_b128 v[186:189], v221 offset:54272
	ds_read_b128 v[182:185], v223 offset:53248
	ds_read_b128 v[190:193], v223 offset:54272
	global_load_lds_dwordx4 v[232:233], off
	s_add_i32 m0, s34, 0x2000
	s_add_u32 s30, s30, 0x40080
	v_lshl_add_u64 v[232:233], v[234:235], 0, s[12:13]
	s_addc_u32 s31, s31, 0
	s_add_i32 s34, s64, s38
	global_load_lds_dwordx4 v[232:233], off
	v_lshl_add_u64 v[232:233], s[30:31], 0, v[194:195]
	s_mov_b32 m0, s34
	s_nop 0
	global_load_lds_dwordx4 v[232:233], off
	v_lshl_add_u64 v[232:233], s[30:31], 0, v[196:197]
	s_add_i32 m0, s34, 0x2000
	s_nop 0
	global_load_lds_dwordx4 v[232:233], off
	s_waitcnt vmcnt(6)
	s_waitcnt lgkmcnt(0)
	s_barrier
	s_setprio 1
	s_waitcnt lgkmcnt(0)
	v_mfma_scale_f32_32x32x64_f8f6f4 v[50:65], v[130:137], v[162:169], v[50:65], v224, v224 op_sel_hi:[0,0,0]
	v_mfma_scale_f32_32x32x64_f8f6f4 v[18:33], v[130:137], v[178:185], v[18:33], v224, v224 op_sel_hi:[0,0,0]
	v_mfma_scale_f32_32x32x64_f8f6f4 v[50:65], v[138:145], v[170:177], v[50:65], v224, v224 op_sel_hi:[0,0,0]
	v_lshl_add_u64 v[232:233], v[236:237], 0, s[12:13]
	s_mov_b32 m0, s50
	s_nop 0
	global_load_lds_dwordx4 v[232:233], off
	v_mfma_scale_f32_32x32x64_f8f6f4 v[18:33], v[138:145], v[186:193], v[18:33], v224, v224 op_sel_hi:[0,0,0]
	v_mfma_scale_f32_32x32x64_f8f6f4 v[34:49], v[146:153], v[162:169], v[34:49], v224, v224 op_sel_hi:[0,0,0]
	v_mfma_scale_f32_32x32x64_f8f6f4 v[2:17], v[146:153], v[178:185], v[2:17], v224, v224 op_sel_hi:[0,0,0]
	v_lshl_add_u64 v[232:233], v[238:239], 0, s[12:13]
	s_mov_b32 m0, s51
	s_nop 0
	global_load_lds_dwordx4 v[232:233], off
	v_mfma_scale_f32_32x32x64_f8f6f4 v[34:49], v[154:161], v[170:177], v[34:49], v224, v224 op_sel_hi:[0,0,0]
	v_mfma_scale_f32_32x32x64_f8f6f4 v[2:17], v[154:161], v[186:193], v[2:17], v224, v224 op_sel_hi:[0,0,0]
	s_setprio 0
	s_barrier
	s_add_i32 s62, s62, 2
	s_add_u32 s28, s28, 0x100
	s_addc_u32 s29, s29, 0
	s_add_u32 s23, s23, 0x100
	s_addc_u32 s25, s25, 0
	s_cmp_gt_u32 s62, 13
	s_cbranch_scc1 .LBB0_1539

.LBB0_1625:
	ds_read_b128 v[168:171], v150
	ds_read_b128 v[172:175], v151
	ds_read_b128 v[176:179], v152
	ds_read_b128 v[180:183], v153
	ds_read_b128 v[184:187], v154
	ds_read_b128 v[188:191], v155
	ds_read_b128 v[192:195], v156
	ds_read_b128 v[196:199], v157
	s_add_u32 s28, s26, 0xfffe0080
	s_addc_u32 s29, s27, -1
	s_cmp_eq_u32 s56, 4
	s_cselect_b32 s31, s19, s29
	s_cselect_b32 s30, s18, s28
	s_cselect_b32 s29, s21, s25
	s_cselect_b32 s28, s20, s23
	v_lshl_add_u64 v[144:145], s[26:27], 0, v[140:141]
	s_add_i32 m0, s35, 0xc000
	ds_read_b128 v[200:203], v158
	ds_read_b128 v[208:211], v158 offset:1024
	ds_read_b128 v[204:207], v159
	ds_read_b128 v[212:215], v159 offset:1024
	ds_read_b128 v[216:219], v158 offset:4096
	ds_read_b128 v[224:227], v158 offset:5120
	ds_read_b128 v[220:223], v159 offset:4096
	ds_read_b128 v[228:231], v159 offset:5120
	global_load_lds_dwordx4 v[144:145], off
	v_lshl_add_u64 v[144:145], s[26:27], 0, v[142:143]
	s_add_i32 m0, s35, 0xe000
	s_nop 0
	global_load_lds_dwordx4 v[144:145], off
	s_waitcnt vmcnt(8)
	s_waitcnt lgkmcnt(0)
	s_barrier
	s_setprio 1
	s_waitcnt lgkmcnt(0)
	v_mfma_scale_f32_32x32x64_f8f6f4 v[114:129], v[168:175], v[200:207], v[114:129], v160, v160 op_sel_hi:[0,0,0]
	v_mfma_scale_f32_32x32x64_f8f6f4 v[82:97], v[168:175], v[216:223], v[82:97], v160, v160 op_sel_hi:[0,0,0]
	v_mfma_scale_f32_32x32x64_f8f6f4 v[114:129], v[176:183], v[208:215], v[114:129], v160, v160 op_sel_hi:[0,0,0]
	v_mfma_scale_f32_32x32x64_f8f6f4 v[82:97], v[176:183], v[224:231], v[82:97], v160, v160 op_sel_hi:[0,0,0]
	v_mfma_scale_f32_32x32x64_f8f6f4 v[98:113], v[184:191], v[200:207], v[98:113], v160, v160 op_sel_hi:[0,0,0]
	v_mfma_scale_f32_32x32x64_f8f6f4 v[66:81], v[184:191], v[216:223], v[66:81], v160, v160 op_sel_hi:[0,0,0]
	v_mfma_scale_f32_32x32x64_f8f6f4 v[98:113], v[192:199], v[208:215], v[98:113], v160, v160 op_sel_hi:[0,0,0]
	v_mfma_scale_f32_32x32x64_f8f6f4 v[66:81], v[192:199], v[224:231], v[66:81], v160, v160 op_sel_hi:[0,0,0]
	s_setprio 0
	s_barrier
	s_add_i32 s57, s49, s34
	v_lshl_add_u64 v[144:145], s[28:29], 0, v[132:133]
	s_mov_b32 m0, s57
	ds_read_b128 v[200:203], v158 offset:16384
	ds_read_b128 v[208:211], v158 offset:17408
	ds_read_b128 v[204:207], v159 offset:16384
	ds_read_b128 v[212:215], v159 offset:17408
	ds_read_b128 v[216:219], v158 offset:20480
	ds_read_b128 v[224:227], v158 offset:21504
	ds_read_b128 v[220:223], v159 offset:20480
	ds_read_b128 v[228:231], v159 offset:21504
	global_load_lds_dwordx4 v[144:145], off
	s_add_i32 m0, s57, 0x2000
	s_add_u32 s58, s28, 0x20000
	v_lshl_add_u64 v[146:147], s[28:29], 0, v[136:137]
	s_addc_u32 s59, s29, 0
	s_add_i32 s57, s50, s34
	global_load_lds_dwordx4 v[146:147], off
	v_lshl_add_u64 v[232:233], s[58:59], 0, v[132:133]
	s_mov_b32 m0, s57
	v_lshl_add_u64 v[234:235], s[30:31], 0, v[134:135]
	global_load_lds_dwordx4 v[232:233], off
	v_lshl_add_u64 v[232:233], s[58:59], 0, v[136:137]
	s_add_i32 m0, s57, 0x2000
	s_nop 0
	global_load_lds_dwordx4 v[232:233], off
	s_waitcnt vmcnt(6)
	s_waitcnt lgkmcnt(0)
	s_barrier
	s_setprio 1
	s_waitcnt lgkmcnt(0)
	v_mfma_scale_f32_32x32x64_f8f6f4 v[50:65], v[168:175], v[200:207], v[50:65], v160, v160 op_sel_hi:[0,0,0]
	v_mfma_scale_f32_32x32x64_f8f6f4 v[18:33], v[168:175], v[216:223], v[18:33], v160, v160 op_sel_hi:[0,0,0]
	v_mfma_scale_f32_32x32x64_f8f6f4 v[50:65], v[176:183], v[208:215], v[50:65], v160, v160 op_sel_hi:[0,0,0]
	v_lshl_add_u64 v[232:233], s[30:31], 0, v[130:131]
	s_mov_b32 m0, s35
	s_nop 0
	global_load_lds_dwordx4 v[232:233], off
	v_mfma_scale_f32_32x32x64_f8f6f4 v[18:33], v[176:183], v[224:231], v[18:33], v160, v160 op_sel_hi:[0,0,0]
	v_mfma_scale_f32_32x32x64_f8f6f4 v[34:49], v[184:191], v[200:207], v[34:49], v160, v160 op_sel_hi:[0,0,0]
	v_mfma_scale_f32_32x32x64_f8f6f4 v[2:17], v[184:191], v[216:223], v[2:17], v160, v160 op_sel_hi:[0,0,0]
	s_mov_b32 m0, s36
	s_nop 0
	global_load_lds_dwordx4 v[234:235], off
	v_mfma_scale_f32_32x32x64_f8f6f4 v[34:49], v[192:199], v[208:215], v[34:49], v160, v160 op_sel_hi:[0,0,0]
	v_mfma_scale_f32_32x32x64_f8f6f4 v[2:17], v[192:199], v[224:231], v[2:17], v160, v160 op_sel_hi:[0,0,0]
	s_setprio 0
	s_barrier
	s_add_i32 s57, 0, 0x18000
	v_add_u32_e32 v167, s57, v1
	v_add_u32_e32 v172, s57, v148
	s_add_i32 s58, 0, 0x1c000
	ds_read_b128 v[168:171], v167
	ds_read_b128 v[172:175], v172
	ds_read_b128 v[176:179], v161
	ds_read_b128 v[180:183], v162
	v_add_u32_e32 v167, s58, v1
	v_add_u32_e32 v188, s58, v148
	ds_read_b128 v[184:187], v167
	ds_read_b128 v[188:191], v188
	ds_read_b128 v[192:195], v163
	ds_read_b128 v[196:199], v164
	s_add_u32 s30, s30, 0x20000
	s_addc_u32 s31, s31, 0
	s_mov_b32 m0, s37
	v_lshl_add_u64 v[236:237], s[30:31], 0, v[130:131]
	ds_read_b128 v[200:203], v158 offset:32768
	ds_read_b128 v[208:211], v158 offset:33792
	ds_read_b128 v[204:207], v159 offset:32768
	ds_read_b128 v[212:215], v159 offset:33792
	ds_read_b128 v[216:219], v158 offset:36864
	ds_read_b128 v[224:227], v158 offset:37888
	ds_read_b128 v[220:223], v159 offset:36864
	ds_read_b128 v[228:231], v159 offset:37888
	global_load_lds_dwordx4 v[236:237], off
	v_lshl_add_u64 v[236:237], s[30:31], 0, v[134:135]
	s_mov_b32 m0, s38
	s_nop 0
	global_load_lds_dwordx4 v[236:237], off
	s_waitcnt vmcnt(8)
	s_waitcnt lgkmcnt(0)
	s_barrier
	s_setprio 1
	s_waitcnt lgkmcnt(0)
	v_mfma_scale_f32_32x32x64_f8f6f4 v[114:129], v[168:175], v[200:207], v[114:129], v160, v160 op_sel_hi:[0,0,0]
	v_mfma_scale_f32_32x32x64_f8f6f4 v[82:97], v[168:175], v[216:223], v[82:97], v160, v160 op_sel_hi:[0,0,0]
	v_mfma_scale_f32_32x32x64_f8f6f4 v[114:129], v[176:183], v[208:215], v[114:129], v160, v160 op_sel_hi:[0,0,0]
	v_mfma_scale_f32_32x32x64_f8f6f4 v[82:97], v[176:183], v[224:231], v[82:97], v160, v160 op_sel_hi:[0,0,0]
	v_mfma_scale_f32_32x32x64_f8f6f4 v[98:113], v[184:191], v[200:207], v[98:113], v160, v160 op_sel_hi:[0,0,0]
	v_mfma_scale_f32_32x32x64_f8f6f4 v[66:81], v[184:191], v[216:223], v[66:81], v160, v160 op_sel_hi:[0,0,0]
	v_mfma_scale_f32_32x32x64_f8f6f4 v[98:113], v[192:199], v[208:215], v[98:113], v160, v160 op_sel_hi:[0,0,0]
	v_mfma_scale_f32_32x32x64_f8f6f4 v[66:81], v[192:199], v[224:231], v[66:81], v160, v160 op_sel_hi:[0,0,0]
	s_setprio 0
	s_barrier
	s_add_i32 s30, s57, s34
	v_lshl_add_u64 v[144:145], v[144:145], 0, s[10:11]
	s_mov_b32 m0, s30
	ds_read_b128 v[200:203], v158 offset:49152
	ds_read_b128 v[208:211], v158 offset:50176
	ds_read_b128 v[204:207], v159 offset:49152
	ds_read_b128 v[212:215], v159 offset:50176
	ds_read_b128 v[216:219], v158 offset:53248
	ds_read_b128 v[224:227], v158 offset:54272
	ds_read_b128 v[220:223], v159 offset:53248
	ds_read_b128 v[228:231], v159 offset:54272
	global_load_lds_dwordx4 v[144:145], off
	s_add_i32 m0, s30, 0x2000
	s_add_u32 s28, s28, 0x20080
	v_lshl_add_u64 v[144:145], v[146:147], 0, s[10:11]
	s_addc_u32 s29, s29, 0
	s_add_i32 s30, s58, s34
	global_load_lds_dwordx4 v[144:145], off
	v_lshl_add_u64 v[144:145], s[28:29], 0, v[132:133]
	s_mov_b32 m0, s30
	s_nop 0
	global_load_lds_dwordx4 v[144:145], off
	v_lshl_add_u64 v[144:145], s[28:29], 0, v[136:137]
	s_add_i32 m0, s30, 0x2000
	s_nop 0
	global_load_lds_dwordx4 v[144:145], off
	s_waitcnt vmcnt(6)
	s_waitcnt lgkmcnt(0)
	s_barrier
	s_setprio 1
	s_waitcnt lgkmcnt(0)
	v_mfma_scale_f32_32x32x64_f8f6f4 v[50:65], v[168:175], v[200:207], v[50:65], v160, v160 op_sel_hi:[0,0,0]
	v_mfma_scale_f32_32x32x64_f8f6f4 v[18:33], v[168:175], v[216:223], v[18:33], v160, v160 op_sel_hi:[0,0,0]
	v_mfma_scale_f32_32x32x64_f8f6f4 v[50:65], v[176:183], v[208:215], v[50:65], v160, v160 op_sel_hi:[0,0,0]
	v_lshl_add_u64 v[144:145], v[232:233], 0, s[10:11]
	s_mov_b32 m0, s44
	s_nop 0
	global_load_lds_dwordx4 v[144:145], off
	v_mfma_scale_f32_32x32x64_f8f6f4 v[18:33], v[176:183], v[224:231], v[18:33], v160, v160 op_sel_hi:[0,0,0]
	v_mfma_scale_f32_32x32x64_f8f6f4 v[34:49], v[184:191], v[200:207], v[34:49], v160, v160 op_sel_hi:[0,0,0]
	v_mfma_scale_f32_32x32x64_f8f6f4 v[2:17], v[184:191], v[216:223], v[2:17], v160, v160 op_sel_hi:[0,0,0]
	v_lshl_add_u64 v[144:145], v[234:235], 0, s[10:11]
	s_mov_b32 m0, s45
	s_nop 0
	global_load_lds_dwordx4 v[144:145], off
	v_mfma_scale_f32_32x32x64_f8f6f4 v[34:49], v[192:199], v[208:215], v[34:49], v160, v160 op_sel_hi:[0,0,0]
	v_mfma_scale_f32_32x32x64_f8f6f4 v[2:17], v[192:199], v[224:231], v[2:17], v160, v160 op_sel_hi:[0,0,0]
	s_setprio 0
	s_barrier
	s_add_i32 s56, s56, 2
	s_add_u32 s26, s26, 0x100
	s_addc_u32 s27, s27, 0
	s_add_u32 s23, s23, 0x100
	s_addc_u32 s25, s25, 0
	s_cmp_gt_u32 s56, 5
	s_cbranch_scc0 .LBB0_1625
	s_and_b64 vcc, exec, s[12:13]
	s_cbranch_vccz .LBB0_1628
	s_barrier
